# first-trip waits counted past the previous epilogue stores (exact per path), no early retire at epilogue end; GU index-load wait counted
# baseline (speedup 1.0000x reference)
.LBB0_87:
	s_andn2_b64 vcc, exec, s[22:23]
	s_cbranch_vccnz .LBB0_90
	s_add_u32 s46, s46, 0x80
	s_addc_u32 s47, s47, 0
	s_add_u32 s27, s48, 0x100
	s_addc_u32 s29, s49, 0
	s_mov_b32 s4, 0
	s_add_i32 s48, s4, 2
	s_add_u32 s49, s46, 0x80
	s_addc_u32 s5, s47, 0
	s_add_i32 s77, 0, 0x10000
	s_cmp_eq_u32 s72, s4
	s_cselect_b32 s5, s43, s5
	s_cselect_b32 s4, s42, s49
	v_add_u32_e32 v149, s77, v145
	s_cselect_b32 s83, s45, s29
	s_cselect_b32 s82, s44, s27
	s_add_i32 s49, 0, 0x14000
	ds_read_b128 v[140:143], v149
	ds_read_b128 v[150:153], v149 offset:1024
	ds_read_b128 v[154:157], v149 offset:2048
	ds_read_b128 v[158:161], v149 offset:3072
	v_add_u32_e32 v149, s49, v145
	ds_read_b128 v[162:165], v149
	ds_read_b128 v[166:169], v149 offset:1024
	ds_read_b128 v[170:173], v149 offset:2048
	ds_read_b128 v[174:177], v149 offset:3072
	v_lshl_add_u64 v[214:215], s[46:47], 0, v[136:137]
	s_add_i32 m0, s37, 0xc000
	ds_read_b128 v[178:181], v148
	ds_read_b128 v[182:185], v148 offset:1024
	ds_read_b128 v[186:189], v148 offset:2048
	ds_read_b128 v[190:193], v148 offset:3072
	ds_read_b128 v[194:197], v148 offset:4096
	ds_read_b128 v[202:205], v148 offset:5120
	ds_read_b128 v[206:209], v148 offset:6144
	ds_read_b128 v[210:213], v148 offset:7168
	global_load_lds_dwordx4 v[214:215], off
	v_lshl_add_u64 v[214:215], s[46:47], 0, v[138:139]
	s_add_i32 m0, s37, 0xe000
	s_nop 0
	global_load_lds_dwordx4 v[214:215], off
	s_cmp_lg_u32 s32, 0
	s_cbranch_scc1 .Lfw_ip_a24
	s_waitcnt vmcnt(16)
	s_branch .Lfw_ip_ad
.Lfw_ip_a24:
	s_waitcnt vmcnt(24)
.Lfw_ip_ad:
	s_waitcnt lgkmcnt(0)
	s_barrier
	s_setprio 1
	s_waitcnt lgkmcnt(0)
	v_mfma_f32_16x16x32_bf16 v[122:125], v[140:143], v[178:181], 0
	v_mfma_f32_16x16x32_bf16 v[126:129], v[154:157], v[178:181], 0
	v_mfma_f32_16x16x32_bf16 v[110:113], v[140:143], v[186:189], 0
	v_mfma_f32_16x16x32_bf16 v[106:109], v[154:157], v[186:189], 0
	v_mfma_f32_16x16x32_bf16 v[94:97], v[140:143], v[194:197], 0
	v_mfma_f32_16x16x32_bf16 v[90:93], v[154:157], v[194:197], 0
	v_mfma_f32_16x16x32_bf16 v[78:81], v[140:143], v[206:209], 0
	v_mfma_f32_16x16x32_bf16 v[74:77], v[154:157], v[206:209], 0
	v_mfma_f32_16x16x32_bf16 v[122:125], v[150:153], v[182:185], v[122:125]
	v_mfma_f32_16x16x32_bf16 v[126:129], v[158:161], v[182:185], v[126:129]
	v_mfma_f32_16x16x32_bf16 v[110:113], v[150:153], v[190:193], v[110:113]
	v_mfma_f32_16x16x32_bf16 v[106:109], v[158:161], v[190:193], v[106:109]
	v_mfma_f32_16x16x32_bf16 v[94:97], v[150:153], v[202:205], v[94:97]
	v_mfma_f32_16x16x32_bf16 v[90:93], v[158:161], v[202:205], v[90:93]
	v_mfma_f32_16x16x32_bf16 v[78:81], v[150:153], v[210:213], v[78:81]
	v_mfma_f32_16x16x32_bf16 v[74:77], v[158:161], v[210:213], v[74:77]
	s_setprio 0
	s_setprio 1
	v_mfma_f32_16x16x32_bf16 v[118:121], v[162:165], v[178:181], 0
	v_mfma_f32_16x16x32_bf16 v[114:117], v[170:173], v[178:181], 0
	v_mfma_f32_16x16x32_bf16 v[102:105], v[162:165], v[186:189], 0
	v_mfma_f32_16x16x32_bf16 v[98:101], v[170:173], v[186:189], 0
	v_mfma_f32_16x16x32_bf16 v[86:89], v[162:165], v[194:197], 0
	v_mfma_f32_16x16x32_bf16 v[82:85], v[170:173], v[194:197], 0
	v_mfma_f32_16x16x32_bf16 v[70:73], v[162:165], v[206:209], 0
	v_mfma_f32_16x16x32_bf16 v[66:69], v[170:173], v[206:209], 0
	v_mfma_f32_16x16x32_bf16 v[118:121], v[166:169], v[182:185], v[118:121]
	v_mfma_f32_16x16x32_bf16 v[114:117], v[174:177], v[182:185], v[114:117]
	v_mfma_f32_16x16x32_bf16 v[102:105], v[166:169], v[190:193], v[102:105]
	v_mfma_f32_16x16x32_bf16 v[98:101], v[174:177], v[190:193], v[98:101]
	v_mfma_f32_16x16x32_bf16 v[86:89], v[166:169], v[202:205], v[86:89]
	v_mfma_f32_16x16x32_bf16 v[82:85], v[174:177], v[202:205], v[82:85]
	v_mfma_f32_16x16x32_bf16 v[70:73], v[166:169], v[210:213], v[70:73]
	v_mfma_f32_16x16x32_bf16 v[66:69], v[174:177], v[210:213], v[66:69]
	s_setprio 0
	s_barrier
	s_add_i32 s77, s77, s51
	v_lshl_add_u64 v[214:215], s[82:83], 0, v[0:1]
	s_mov_b32 m0, s77
	ds_read_b128 v[178:181], v148 offset:16384
	ds_read_b128 v[182:185], v148 offset:17408
	ds_read_b128 v[186:189], v148 offset:18432
	ds_read_b128 v[190:193], v148 offset:19456
	ds_read_b128 v[194:197], v148 offset:20480
	ds_read_b128 v[202:205], v148 offset:21504
	ds_read_b128 v[206:209], v148 offset:22528
	ds_read_b128 v[210:213], v148 offset:23552
	global_load_lds_dwordx4 v[214:215], off
	s_add_i32 m0, s77, 0x2000
	v_lshl_add_u64 v[216:217], s[82:83], 0, v[130:131]
	s_add_u32 s82, s82, s14
	s_addc_u32 s83, s83, s15
	s_add_i32 s49, s49, s51
	global_load_lds_dwordx4 v[216:217], off
	v_lshl_add_u64 v[218:219], s[82:83], 0, v[0:1]
	s_mov_b32 m0, s49
	v_lshl_add_u64 v[220:221], s[82:83], 0, v[130:131]
	global_load_lds_dwordx4 v[218:219], off
	s_add_i32 m0, s49, 0x2000
	v_lshl_add_u64 v[234:235], s[4:5], 0, v[132:133]
	global_load_lds_dwordx4 v[220:221], off
	s_mov_b32 m0, s37
	v_lshl_add_u64 v[236:237], s[4:5], 0, v[134:135]
	global_load_lds_dwordx4 v[234:235], off
	s_mov_b32 m0, s41
	s_nop 0
	global_load_lds_dwordx4 v[236:237], off
	s_cmp_eq_u32 s76, 1
	s_cbranch_scc1 .Lfw_ip_8
	s_cmp_lg_u32 s32, 0
	s_cbranch_scc1 .Lfw_ip_b24
	s_waitcnt vmcnt(16)
	s_branch .Lfw_ip_bd
.Lfw_ip_b24:
	s_waitcnt vmcnt(24)
	s_branch .Lfw_ip_bd
.Lfw_ip_8:
	s_waitcnt vmcnt(8)
.Lfw_ip_bd:
	s_waitcnt lgkmcnt(0)
	s_barrier
	s_setprio 1
	s_waitcnt lgkmcnt(0)
	v_mfma_f32_16x16x32_bf16 v[62:65], v[140:143], v[178:181], 0
	v_mfma_f32_16x16x32_bf16 v[58:61], v[154:157], v[178:181], 0
	v_mfma_f32_16x16x32_bf16 v[46:49], v[140:143], v[186:189], 0
	v_mfma_f32_16x16x32_bf16 v[42:45], v[154:157], v[186:189], 0
	v_mfma_f32_16x16x32_bf16 v[30:33], v[140:143], v[194:197], 0
	v_mfma_f32_16x16x32_bf16 v[26:29], v[154:157], v[194:197], 0
	v_mfma_f32_16x16x32_bf16 v[14:17], v[140:143], v[206:209], 0
	v_mfma_f32_16x16x32_bf16 v[10:13], v[154:157], v[206:209], 0
	v_mfma_f32_16x16x32_bf16 v[62:65], v[150:153], v[182:185], v[62:65]
	v_mfma_f32_16x16x32_bf16 v[58:61], v[158:161], v[182:185], v[58:61]
	v_mfma_f32_16x16x32_bf16 v[46:49], v[150:153], v[190:193], v[46:49]
	v_mfma_f32_16x16x32_bf16 v[42:45], v[158:161], v[190:193], v[42:45]
	v_mfma_f32_16x16x32_bf16 v[30:33], v[150:153], v[202:205], v[30:33]
	v_mfma_f32_16x16x32_bf16 v[26:29], v[158:161], v[202:205], v[26:29]
	v_mfma_f32_16x16x32_bf16 v[14:17], v[150:153], v[210:213], v[14:17]
	v_mfma_f32_16x16x32_bf16 v[10:13], v[158:161], v[210:213], v[10:13]
	s_setprio 0
	s_setprio 1
	v_mfma_f32_16x16x32_bf16 v[54:57], v[162:165], v[178:181], 0
	v_mfma_f32_16x16x32_bf16 v[50:53], v[170:173], v[178:181], 0
	v_mfma_f32_16x16x32_bf16 v[38:41], v[162:165], v[186:189], 0
	v_mfma_f32_16x16x32_bf16 v[34:37], v[170:173], v[186:189], 0
	v_mfma_f32_16x16x32_bf16 v[22:25], v[162:165], v[194:197], 0
	v_mfma_f32_16x16x32_bf16 v[18:21], v[170:173], v[194:197], 0
	v_mfma_f32_16x16x32_bf16 v[6:9], v[162:165], v[206:209], 0
	v_mfma_f32_16x16x32_bf16 v[2:5], v[170:173], v[206:209], 0
	v_mfma_f32_16x16x32_bf16 v[54:57], v[166:169], v[182:185], v[54:57]
	v_mfma_f32_16x16x32_bf16 v[50:53], v[174:177], v[182:185], v[50:53]
	v_mfma_f32_16x16x32_bf16 v[38:41], v[166:169], v[190:193], v[38:41]
	v_mfma_f32_16x16x32_bf16 v[34:37], v[174:177], v[190:193], v[34:37]
	v_mfma_f32_16x16x32_bf16 v[22:25], v[166:169], v[202:205], v[22:25]
	v_mfma_f32_16x16x32_bf16 v[18:21], v[174:177], v[202:205], v[18:21]
	v_mfma_f32_16x16x32_bf16 v[6:9], v[166:169], v[210:213], v[6:9]
	v_mfma_f32_16x16x32_bf16 v[2:5], v[174:177], v[210:213], v[2:5]
	s_setprio 0
	s_barrier
	s_add_i32 s49, 0, 0x18000
	v_add_u32_e32 v149, s49, v145
	s_add_i32 s77, 0, 0x1c000
	ds_read_b128 v[140:143], v149
	ds_read_b128 v[150:153], v149 offset:1024
	ds_read_b128 v[154:157], v149 offset:2048
	ds_read_b128 v[158:161], v149 offset:3072
	v_add_u32_e32 v149, s77, v145
	ds_read_b128 v[162:165], v149
	ds_read_b128 v[166:169], v149 offset:1024
	ds_read_b128 v[170:173], v149 offset:2048
	ds_read_b128 v[174:177], v149 offset:3072
	s_add_u32 s4, s4, s14
	s_addc_u32 s5, s5, s15
	s_mov_b32 m0, s67
	v_lshl_add_u64 v[238:239], s[4:5], 0, v[132:133]
	ds_read_b128 v[178:181], v148 offset:32768
	ds_read_b128 v[182:185], v148 offset:33792
	ds_read_b128 v[186:189], v148 offset:34816
	ds_read_b128 v[190:193], v148 offset:35840
	ds_read_b128 v[194:197], v148 offset:36864
	ds_read_b128 v[202:205], v148 offset:37888
	ds_read_b128 v[206:209], v148 offset:38912
	ds_read_b128 v[210:213], v148 offset:39936
	global_load_lds_dwordx4 v[238:239], off
	v_lshl_add_u64 v[238:239], s[4:5], 0, v[134:135]
	s_mov_b32 m0, s68
	s_nop 0
	global_load_lds_dwordx4 v[238:239], off
	s_waitcnt vmcnt(8)
	s_waitcnt lgkmcnt(0)
	s_barrier
	s_setprio 1
	s_waitcnt lgkmcnt(0)
	v_mfma_f32_16x16x32_bf16 v[122:125], v[140:143], v[178:181], v[122:125]
	v_mfma_f32_16x16x32_bf16 v[126:129], v[154:157], v[178:181], v[126:129]
	v_mfma_f32_16x16x32_bf16 v[110:113], v[140:143], v[186:189], v[110:113]
	v_mfma_f32_16x16x32_bf16 v[106:109], v[154:157], v[186:189], v[106:109]
	v_mfma_f32_16x16x32_bf16 v[94:97], v[140:143], v[194:197], v[94:97]
	v_mfma_f32_16x16x32_bf16 v[90:93], v[154:157], v[194:197], v[90:93]
	v_mfma_f32_16x16x32_bf16 v[78:81], v[140:143], v[206:209], v[78:81]
	v_mfma_f32_16x16x32_bf16 v[74:77], v[154:157], v[206:209], v[74:77]
	v_mfma_f32_16x16x32_bf16 v[122:125], v[150:153], v[182:185], v[122:125]
	v_mfma_f32_16x16x32_bf16 v[126:129], v[158:161], v[182:185], v[126:129]
	v_mfma_f32_16x16x32_bf16 v[110:113], v[150:153], v[190:193], v[110:113]
	v_mfma_f32_16x16x32_bf16 v[106:109], v[158:161], v[190:193], v[106:109]
	v_mfma_f32_16x16x32_bf16 v[94:97], v[150:153], v[202:205], v[94:97]
	v_mfma_f32_16x16x32_bf16 v[90:93], v[158:161], v[202:205], v[90:93]
	v_mfma_f32_16x16x32_bf16 v[78:81], v[150:153], v[210:213], v[78:81]
	v_mfma_f32_16x16x32_bf16 v[74:77], v[158:161], v[210:213], v[74:77]
	s_setprio 0
	s_setprio 1
	v_mfma_f32_16x16x32_bf16 v[118:121], v[162:165], v[178:181], v[118:121]
	v_mfma_f32_16x16x32_bf16 v[114:117], v[170:173], v[178:181], v[114:117]
	v_mfma_f32_16x16x32_bf16 v[102:105], v[162:165], v[186:189], v[102:105]
	v_mfma_f32_16x16x32_bf16 v[98:101], v[170:173], v[186:189], v[98:101]
	v_mfma_f32_16x16x32_bf16 v[86:89], v[162:165], v[194:197], v[86:89]
	v_mfma_f32_16x16x32_bf16 v[82:85], v[170:173], v[194:197], v[82:85]
	v_mfma_f32_16x16x32_bf16 v[70:73], v[162:165], v[206:209], v[70:73]
	v_mfma_f32_16x16x32_bf16 v[66:69], v[170:173], v[206:209], v[66:69]
	v_mfma_f32_16x16x32_bf16 v[118:121], v[166:169], v[182:185], v[118:121]
	v_mfma_f32_16x16x32_bf16 v[114:117], v[174:177], v[182:185], v[114:117]
	v_mfma_f32_16x16x32_bf16 v[102:105], v[166:169], v[190:193], v[102:105]
	v_mfma_f32_16x16x32_bf16 v[98:101], v[174:177], v[190:193], v[98:101]
	v_mfma_f32_16x16x32_bf16 v[86:89], v[166:169], v[202:205], v[86:89]
	v_mfma_f32_16x16x32_bf16 v[82:85], v[174:177], v[202:205], v[82:85]
	v_mfma_f32_16x16x32_bf16 v[70:73], v[166:169], v[210:213], v[70:73]
	v_mfma_f32_16x16x32_bf16 v[66:69], v[174:177], v[210:213], v[66:69]
	s_setprio 0
	s_barrier
	s_add_i32 s4, s49, s51
	v_lshl_add_u64 v[214:215], v[214:215], 0, s[94:95]
	s_mov_b32 m0, s4
	ds_read_b128 v[178:181], v148 offset:49152
	ds_read_b128 v[182:185], v148 offset:50176
	ds_read_b128 v[186:189], v148 offset:51200
	ds_read_b128 v[190:193], v148 offset:52224
	ds_read_b128 v[194:197], v148 offset:53248
	ds_read_b128 v[202:205], v148 offset:54272
	ds_read_b128 v[206:209], v148 offset:55296
	ds_read_b128 v[210:213], v148 offset:56320
	global_load_lds_dwordx4 v[214:215], off
	v_lshl_add_u64 v[214:215], v[216:217], 0, s[94:95]
	s_add_i32 m0, s4, 0x2000
	s_add_i32 s4, s77, s51
	global_load_lds_dwordx4 v[214:215], off
	v_lshl_add_u64 v[214:215], v[218:219], 0, s[94:95]
	s_mov_b32 m0, s4
	s_nop 0
	global_load_lds_dwordx4 v[214:215], off
	v_lshl_add_u64 v[214:215], v[220:221], 0, s[94:95]
	s_add_i32 m0, s4, 0x2000
	s_nop 0
	global_load_lds_dwordx4 v[214:215], off
	v_lshl_add_u64 v[214:215], v[234:235], 0, s[94:95]
	s_mov_b32 m0, s69
	s_nop 0
	global_load_lds_dwordx4 v[214:215], off
	v_lshl_add_u64 v[214:215], v[236:237], 0, s[94:95]
	s_mov_b32 m0, s70
	s_nop 0
	global_load_lds_dwordx4 v[214:215], off
	s_waitcnt vmcnt(8)
	s_waitcnt lgkmcnt(0)
	s_barrier
	s_setprio 1
	s_waitcnt lgkmcnt(0)
	v_mfma_f32_16x16x32_bf16 v[62:65], v[140:143], v[178:181], v[62:65]
	v_mfma_f32_16x16x32_bf16 v[58:61], v[154:157], v[178:181], v[58:61]
	v_mfma_f32_16x16x32_bf16 v[46:49], v[140:143], v[186:189], v[46:49]
	v_mfma_f32_16x16x32_bf16 v[42:45], v[154:157], v[186:189], v[42:45]
	v_mfma_f32_16x16x32_bf16 v[30:33], v[140:143], v[194:197], v[30:33]
	v_mfma_f32_16x16x32_bf16 v[26:29], v[154:157], v[194:197], v[26:29]
	v_mfma_f32_16x16x32_bf16 v[14:17], v[140:143], v[206:209], v[14:17]
	v_mfma_f32_16x16x32_bf16 v[10:13], v[154:157], v[206:209], v[10:13]
	v_mfma_f32_16x16x32_bf16 v[62:65], v[150:153], v[182:185], v[62:65]
	v_mfma_f32_16x16x32_bf16 v[58:61], v[158:161], v[182:185], v[58:61]
	v_mfma_f32_16x16x32_bf16 v[46:49], v[150:153], v[190:193], v[46:49]
	v_mfma_f32_16x16x32_bf16 v[42:45], v[158:161], v[190:193], v[42:45]
	v_mfma_f32_16x16x32_bf16 v[30:33], v[150:153], v[202:205], v[30:33]
	v_mfma_f32_16x16x32_bf16 v[26:29], v[158:161], v[202:205], v[26:29]
	v_mfma_f32_16x16x32_bf16 v[14:17], v[150:153], v[210:213], v[14:17]
	v_mfma_f32_16x16x32_bf16 v[10:13], v[158:161], v[210:213], v[10:13]
	s_setprio 0
	s_setprio 1
	v_mfma_f32_16x16x32_bf16 v[54:57], v[162:165], v[178:181], v[54:57]
	v_mfma_f32_16x16x32_bf16 v[50:53], v[170:173], v[178:181], v[50:53]
	v_mfma_f32_16x16x32_bf16 v[38:41], v[162:165], v[186:189], v[38:41]
	v_mfma_f32_16x16x32_bf16 v[34:37], v[170:173], v[186:189], v[34:37]
	v_mfma_f32_16x16x32_bf16 v[22:25], v[162:165], v[194:197], v[22:25]
	v_mfma_f32_16x16x32_bf16 v[18:21], v[170:173], v[194:197], v[18:21]
	v_mfma_f32_16x16x32_bf16 v[6:9], v[162:165], v[206:209], v[6:9]
	v_mfma_f32_16x16x32_bf16 v[2:5], v[170:173], v[206:209], v[2:5]
	v_mfma_f32_16x16x32_bf16 v[54:57], v[166:169], v[182:185], v[54:57]
	v_mfma_f32_16x16x32_bf16 v[50:53], v[174:177], v[182:185], v[50:53]
	v_mfma_f32_16x16x32_bf16 v[38:41], v[166:169], v[190:193], v[38:41]
	v_mfma_f32_16x16x32_bf16 v[34:37], v[174:177], v[190:193], v[34:37]
	v_mfma_f32_16x16x32_bf16 v[22:25], v[166:169], v[202:205], v[22:25]
	v_mfma_f32_16x16x32_bf16 v[18:21], v[174:177], v[202:205], v[18:21]
	v_mfma_f32_16x16x32_bf16 v[6:9], v[166:169], v[210:213], v[6:9]
	v_mfma_f32_16x16x32_bf16 v[2:5], v[174:177], v[210:213], v[2:5]
	s_setprio 0
	s_barrier
	s_add_u32 s46, s46, 0x100
	s_addc_u32 s47, s47, 0
	s_add_u32 s27, s27, 0x100
	s_addc_u32 s29, s29, 0
	s_cmp_ge_i32 s48, s71
	s_mov_b32 s4, s48
	s_cbranch_scc1 .LBB0_90

.LBB0_95:
	v_mul_f32_e32 v154, 0xbfb8aa3b, v126
	v_exp_f32_e32 v154, v154
	v_mul_f32_e32 v156, 0xbfb8aa3b, v127
	v_exp_f32_e32 v156, v156
	v_mul_f32_e32 v160, 0xbfb8aa3b, v128
	v_add_f32_e32 v154, 1.0, v154
	v_rcp_f32_e32 v154, v154
	v_exp_f32_e32 v160, v160
	v_mul_f32_e32 v140, 0xbfb8aa3b, v122
	v_mul_f32_e32 v155, 0xbfb8aa3b, v123
	v_fma_f32 v154, v154, s92, 0.5
	v_max_f32_e32 v154, 1.0, v154
	v_cvt_u32_f32_e32 v157, v154
	v_add_f32_e32 v154, 1.0, v156
	v_rcp_f32_e32 v154, v154
	v_exp_f32_e32 v153, v140
	v_exp_f32_e32 v155, v155
	v_mul_f32_e32 v156, 0xbfb8aa3b, v124
	v_fma_f32 v154, v154, s92, 0.5
	v_max_f32_e32 v154, 1.0, v154
	v_cvt_u32_f32_e32 v161, v154
	v_add_f32_e32 v154, 1.0, v160
	v_mul_f32_e32 v160, 0xbfb8aa3b, v125
	v_exp_f32_e32 v156, v156
	v_exp_f32_e32 v160, v160
	v_rcp_f32_e32 v154, v154
	v_add_f32_e32 v153, 1.0, v153
	v_add_f32_e32 v155, 1.0, v155
	v_mul_f32_e32 v162, 0xbfb8aa3b, v129
	v_rcp_f32_e32 v153, v153
	v_rcp_f32_e32 v155, v155
	v_add_f32_e32 v156, 1.0, v156
	v_exp_f32_e32 v162, v162
	v_add_f32_e32 v160, 1.0, v160
	v_rcp_f32_e32 v156, v156
	v_rcp_f32_e32 v160, v160
	v_fma_f32 v154, v154, s92, 0.5
	v_max_f32_e32 v154, 1.0, v154
	v_fma_f32 v153, v153, s92, 0.5
	v_fma_f32 v155, v155, s92, 0.5
	v_cvt_u32_f32_sdwa v163, v154 dst_sel:WORD_1 dst_unused:UNUSED_PAD src0_sel:DWORD
	v_add_f32_e32 v154, 1.0, v162
	v_max_f32_e32 v153, 1.0, v153
	v_max_f32_e32 v155, 1.0, v155
	v_fma_f32 v156, v156, s92, 0.5
	v_rcp_f32_e32 v154, v154
	v_fma_f32 v160, v160, s92, 0.5
	v_cvt_u32_f32_e32 v153, v153
	v_cvt_u32_f32_e32 v155, v155
	v_max_f32_e32 v156, 1.0, v156
	v_max_f32_e32 v160, 1.0, v160
	v_cvt_u32_f32_sdwa v156, v156 dst_sel:WORD_1 dst_unused:UNUSED_PAD src0_sel:DWORD
	v_cvt_u32_f32_sdwa v160, v160 dst_sel:BYTE_3 dst_unused:UNUSED_PAD src0_sel:DWORD
	v_fma_f32 v154, v154, s92, 0.5
	v_max_f32_e32 v154, 1.0, v154
	v_lshl_or_b32 v153, v155, 8, v153
	v_cvt_u32_f32_sdwa v162, v154 dst_sel:BYTE_3 dst_unused:UNUSED_PAD src0_sel:DWORD
	v_or3_b32 v154, v153, v156, v160
	v_mul_f32_e32 v156, 0xbfb8aa3b, v114
	v_exp_f32_e32 v156, v156
	v_mul_f32_e32 v160, 0xbfb8aa3b, v115
	v_exp_f32_e32 v160, v160
	v_lshl_or_b32 v155, v161, 8, v157
	v_add_f32_e32 v156, 1.0, v156
	v_rcp_f32_e32 v156, v156
	v_or3_b32 v155, v155, v163, v162
	v_mul_f32_e32 v162, 0xbfb8aa3b, v116
	v_exp_f32_e32 v162, v162
	v_fma_f32 v156, v156, s92, 0.5
	v_max_f32_e32 v156, 1.0, v156
	v_cvt_u32_f32_e32 v161, v156
	v_add_f32_e32 v156, 1.0, v160
	v_rcp_f32_e32 v156, v156
	v_mul_f32_e32 v153, 0xbfb8aa3b, v118
	v_mul_f32_e32 v157, 0xbfb8aa3b, v119
	v_exp_f32_e32 v153, v153
	v_fma_f32 v156, v156, s92, 0.5
	v_max_f32_e32 v156, 1.0, v156
	v_cvt_u32_f32_e32 v163, v156
	v_add_f32_e32 v156, 1.0, v162
	v_exp_f32_e32 v157, v157
	v_mul_f32_e32 v160, 0xbfb8aa3b, v120
	v_rcp_f32_e32 v156, v156
	v_mul_f32_e32 v162, 0xbfb8aa3b, v121
	v_exp_f32_e32 v160, v160
	v_exp_f32_e32 v162, v162
	v_mul_f32_e32 v164, 0xbfb8aa3b, v117
	v_exp_f32_e32 v164, v164
	v_add_f32_e32 v153, 1.0, v153
	v_add_f32_e32 v157, 1.0, v157
	v_fma_f32 v156, v156, s92, 0.5
	v_rcp_f32_e32 v153, v153
	v_rcp_f32_e32 v157, v157
	v_add_f32_e32 v160, 1.0, v160
	v_max_f32_e32 v156, 1.0, v156
	v_add_f32_e32 v162, 1.0, v162
	v_rcp_f32_e32 v160, v160
	v_rcp_f32_e32 v162, v162
	v_cvt_u32_f32_sdwa v165, v156 dst_sel:WORD_1 dst_unused:UNUSED_PAD src0_sel:DWORD
	v_add_f32_e32 v156, 1.0, v164
	v_rcp_f32_e32 v156, v156
	v_fma_f32 v153, v153, s92, 0.5
	v_fma_f32 v157, v157, s92, 0.5
	v_max_f32_e32 v153, 1.0, v153
	v_max_f32_e32 v157, 1.0, v157
	v_fma_f32 v160, v160, s92, 0.5
	v_fma_f32 v162, v162, s92, 0.5
	v_cvt_u32_f32_e32 v153, v153
	v_cvt_u32_f32_e32 v157, v157
	v_max_f32_e32 v160, 1.0, v160
	v_max_f32_e32 v162, 1.0, v162
	v_fma_f32 v156, v156, s92, 0.5
	v_cvt_u32_f32_sdwa v160, v160 dst_sel:WORD_1 dst_unused:UNUSED_PAD src0_sel:DWORD
	v_cvt_u32_f32_sdwa v162, v162 dst_sel:BYTE_3 dst_unused:UNUSED_PAD src0_sel:DWORD
	v_max_f32_e32 v156, 1.0, v156
	v_cvt_u32_f32_sdwa v164, v156 dst_sel:BYTE_3 dst_unused:UNUSED_PAD src0_sel:DWORD
	v_add_u32_e32 v140, s27, v146
	v_mov_b64_e32 v[142:143], s[20:21]
	v_lshl_or_b32 v153, v157, 8, v153
	v_ashrrev_i32_e32 v141, 31, v140
	v_mad_i64_i32 v[158:159], s[4:5], v149, s79, v[142:143]
	v_or3_b32 v156, v153, v160, v162
	v_lshl_or_b32 v153, v163, 8, v161
	v_mul_f32_e32 v157, 0xbfb8aa3b, v110
	v_exp_f32_e32 v160, v157
	v_or3_b32 v157, v153, v165, v164
	v_lshl_add_u64 v[158:159], v[158:159], 0, v[140:141]
	global_store_dwordx4 v[158:159], v[154:157], off
	v_add_f32_e32 v153, 1.0, v160
	v_mul_f32_e32 v160, 0xbfb8aa3b, v108
	v_mul_f32_e32 v154, 0xbfb8aa3b, v106
	v_exp_f32_e32 v154, v154
	v_mul_f32_e32 v156, 0xbfb8aa3b, v107
	v_exp_f32_e32 v156, v156
	v_exp_f32_e32 v160, v160
	v_add_f32_e32 v154, 1.0, v154
	v_rcp_f32_e32 v154, v154
	v_mul_f32_e32 v155, 0xbfb8aa3b, v111
	v_exp_f32_e32 v155, v155
	v_mul_f32_e32 v162, 0xbfb8aa3b, v109
	v_fma_f32 v154, v154, s92, 0.5
	v_max_f32_e32 v154, 1.0, v154
	v_cvt_u32_f32_e32 v157, v154
	v_add_f32_e32 v154, 1.0, v156
	v_rcp_f32_e32 v154, v154
	v_mul_f32_e32 v156, 0xbfb8aa3b, v112
	v_exp_f32_e32 v156, v156
	v_add_f32_e32 v155, 1.0, v155
	v_fma_f32 v154, v154, s92, 0.5
	v_max_f32_e32 v154, 1.0, v154
	v_cvt_u32_f32_e32 v161, v154
	v_add_f32_e32 v154, 1.0, v160
	v_mul_f32_e32 v160, 0xbfb8aa3b, v113
	v_exp_f32_e32 v160, v160
	v_rcp_f32_e32 v154, v154
	v_rcp_f32_e32 v153, v153
	v_rcp_f32_e32 v155, v155
	v_add_f32_e32 v156, 1.0, v156
	v_exp_f32_e32 v162, v162
	v_add_f32_e32 v160, 1.0, v160
	v_rcp_f32_e32 v156, v156
	v_rcp_f32_e32 v160, v160
	v_fma_f32 v154, v154, s92, 0.5
	v_max_f32_e32 v154, 1.0, v154
	v_fma_f32 v153, v153, s92, 0.5
	v_fma_f32 v155, v155, s92, 0.5
	v_cvt_u32_f32_sdwa v163, v154 dst_sel:WORD_1 dst_unused:UNUSED_PAD src0_sel:DWORD
	v_add_f32_e32 v154, 1.0, v162
	v_max_f32_e32 v153, 1.0, v153
	v_max_f32_e32 v155, 1.0, v155
	v_fma_f32 v156, v156, s92, 0.5
	v_rcp_f32_e32 v154, v154
	v_fma_f32 v160, v160, s92, 0.5
	v_cvt_u32_f32_e32 v153, v153
	v_cvt_u32_f32_e32 v155, v155
	v_max_f32_e32 v156, 1.0, v156
	v_max_f32_e32 v160, 1.0, v160
	v_cvt_u32_f32_sdwa v156, v156 dst_sel:WORD_1 dst_unused:UNUSED_PAD src0_sel:DWORD
	v_cvt_u32_f32_sdwa v160, v160 dst_sel:BYTE_3 dst_unused:UNUSED_PAD src0_sel:DWORD
	v_fma_f32 v154, v154, s92, 0.5
	v_max_f32_e32 v154, 1.0, v154
	v_lshl_or_b32 v153, v155, 8, v153
	v_cvt_u32_f32_sdwa v162, v154 dst_sel:BYTE_3 dst_unused:UNUSED_PAD src0_sel:DWORD
	v_or3_b32 v154, v153, v156, v160
	v_mul_f32_e32 v156, 0xbfb8aa3b, v98
	v_exp_f32_e32 v156, v156
	v_mul_f32_e32 v160, 0xbfb8aa3b, v99
	v_exp_f32_e32 v160, v160
	v_lshl_or_b32 v155, v161, 8, v157
	v_add_f32_e32 v156, 1.0, v156
	v_rcp_f32_e32 v156, v156
	v_or3_b32 v155, v155, v163, v162
	v_mul_f32_e32 v162, 0xbfb8aa3b, v100
	v_exp_f32_e32 v162, v162
	v_fma_f32 v156, v156, s92, 0.5
	v_max_f32_e32 v156, 1.0, v156
	v_cvt_u32_f32_e32 v161, v156
	v_add_f32_e32 v156, 1.0, v160
	v_rcp_f32_e32 v156, v156
	v_mul_f32_e32 v153, 0xbfb8aa3b, v102
	v_mul_f32_e32 v157, 0xbfb8aa3b, v103
	v_exp_f32_e32 v153, v153
	v_fma_f32 v156, v156, s92, 0.5
	v_max_f32_e32 v156, 1.0, v156
	v_cvt_u32_f32_e32 v163, v156
	v_add_f32_e32 v156, 1.0, v162
	v_exp_f32_e32 v157, v157
	v_mul_f32_e32 v160, 0xbfb8aa3b, v104
	v_rcp_f32_e32 v156, v156
	v_mul_f32_e32 v162, 0xbfb8aa3b, v105
	v_exp_f32_e32 v160, v160
	v_exp_f32_e32 v162, v162
	v_mul_f32_e32 v164, 0xbfb8aa3b, v101
	v_exp_f32_e32 v164, v164
	v_add_f32_e32 v153, 1.0, v153
	v_add_f32_e32 v157, 1.0, v157
	v_fma_f32 v156, v156, s92, 0.5
	v_rcp_f32_e32 v153, v153
	v_rcp_f32_e32 v157, v157
	v_add_f32_e32 v160, 1.0, v160
	v_max_f32_e32 v156, 1.0, v156
	v_add_f32_e32 v162, 1.0, v162
	v_rcp_f32_e32 v160, v160
	v_rcp_f32_e32 v162, v162
	v_cvt_u32_f32_sdwa v165, v156 dst_sel:WORD_1 dst_unused:UNUSED_PAD src0_sel:DWORD
	v_add_f32_e32 v156, 1.0, v164
	v_rcp_f32_e32 v156, v156
	v_fma_f32 v153, v153, s92, 0.5
	v_fma_f32 v157, v157, s92, 0.5
	v_max_f32_e32 v153, 1.0, v153
	v_max_f32_e32 v157, 1.0, v157
	v_fma_f32 v160, v160, s92, 0.5
	v_fma_f32 v162, v162, s92, 0.5
	v_cvt_u32_f32_e32 v153, v153
	v_cvt_u32_f32_e32 v157, v157
	v_max_f32_e32 v160, 1.0, v160
	v_max_f32_e32 v162, 1.0, v162
	v_fma_f32 v156, v156, s92, 0.5
	v_cvt_u32_f32_sdwa v160, v160 dst_sel:WORD_1 dst_unused:UNUSED_PAD src0_sel:DWORD
	v_cvt_u32_f32_sdwa v162, v162 dst_sel:BYTE_3 dst_unused:UNUSED_PAD src0_sel:DWORD
	v_max_f32_e32 v156, 1.0, v156
	v_cvt_u32_f32_sdwa v164, v156 dst_sel:BYTE_3 dst_unused:UNUSED_PAD src0_sel:DWORD
	v_lshl_or_b32 v153, v157, 8, v153
	v_mad_i64_i32 v[158:159], s[4:5], v152, s79, v[142:143]
	v_or3_b32 v156, v153, v160, v162
	v_lshl_or_b32 v153, v163, 8, v161
	v_mul_f32_e32 v157, 0xbfb8aa3b, v94
	v_exp_f32_e32 v160, v157
	v_or3_b32 v157, v153, v165, v164
	v_lshl_add_u64 v[158:159], v[158:159], 0, v[140:141]
	global_store_dwordx4 v[158:159], v[154:157], off
	v_add_f32_e32 v153, 1.0, v160
	v_mul_f32_e32 v160, 0xbfb8aa3b, v92
	v_mul_f32_e32 v154, 0xbfb8aa3b, v90
	v_exp_f32_e32 v154, v154
	v_mul_f32_e32 v156, 0xbfb8aa3b, v91
	v_exp_f32_e32 v156, v156
	v_exp_f32_e32 v160, v160
	v_add_f32_e32 v154, 1.0, v154
	v_rcp_f32_e32 v154, v154
	v_mul_f32_e32 v155, 0xbfb8aa3b, v95
	v_exp_f32_e32 v155, v155
	v_mul_f32_e32 v162, 0xbfb8aa3b, v93
	v_fma_f32 v154, v154, s92, 0.5
	v_max_f32_e32 v154, 1.0, v154
	v_cvt_u32_f32_e32 v157, v154
	v_add_f32_e32 v154, 1.0, v156
	v_rcp_f32_e32 v154, v154
	v_mul_f32_e32 v156, 0xbfb8aa3b, v96
	v_exp_f32_e32 v156, v156
	v_add_f32_e32 v155, 1.0, v155
	v_fma_f32 v154, v154, s92, 0.5
	v_max_f32_e32 v154, 1.0, v154
	v_cvt_u32_f32_e32 v161, v154
	v_add_f32_e32 v154, 1.0, v160
	v_mul_f32_e32 v160, 0xbfb8aa3b, v97
	v_exp_f32_e32 v160, v160
	v_rcp_f32_e32 v154, v154
	v_rcp_f32_e32 v153, v153
	v_rcp_f32_e32 v155, v155
	v_add_f32_e32 v156, 1.0, v156
	v_exp_f32_e32 v162, v162
	v_add_f32_e32 v160, 1.0, v160
	v_rcp_f32_e32 v156, v156
	v_rcp_f32_e32 v160, v160
	v_fma_f32 v154, v154, s92, 0.5
	v_max_f32_e32 v154, 1.0, v154
	v_fma_f32 v153, v153, s92, 0.5
	v_fma_f32 v155, v155, s92, 0.5
	v_cvt_u32_f32_sdwa v163, v154 dst_sel:WORD_1 dst_unused:UNUSED_PAD src0_sel:DWORD
	v_add_f32_e32 v154, 1.0, v162
	v_max_f32_e32 v153, 1.0, v153
	v_max_f32_e32 v155, 1.0, v155
	v_fma_f32 v156, v156, s92, 0.5
	v_rcp_f32_e32 v154, v154
	v_fma_f32 v160, v160, s92, 0.5
	v_cvt_u32_f32_e32 v153, v153
	v_cvt_u32_f32_e32 v155, v155
	v_max_f32_e32 v156, 1.0, v156
	v_max_f32_e32 v160, 1.0, v160
	v_cvt_u32_f32_sdwa v156, v156 dst_sel:WORD_1 dst_unused:UNUSED_PAD src0_sel:DWORD
	v_cvt_u32_f32_sdwa v160, v160 dst_sel:BYTE_3 dst_unused:UNUSED_PAD src0_sel:DWORD
	v_fma_f32 v154, v154, s92, 0.5
	v_max_f32_e32 v154, 1.0, v154
	v_lshl_or_b32 v153, v155, 8, v153
	v_cvt_u32_f32_sdwa v162, v154 dst_sel:BYTE_3 dst_unused:UNUSED_PAD src0_sel:DWORD
	v_or3_b32 v154, v153, v156, v160
	v_mul_f32_e32 v156, 0xbfb8aa3b, v82
	v_exp_f32_e32 v156, v156
	v_mul_f32_e32 v160, 0xbfb8aa3b, v83
	v_exp_f32_e32 v160, v160
	v_lshl_or_b32 v155, v161, 8, v157
	v_add_f32_e32 v156, 1.0, v156
	v_rcp_f32_e32 v156, v156
	v_or3_b32 v155, v155, v163, v162
	v_mul_f32_e32 v162, 0xbfb8aa3b, v84
	v_exp_f32_e32 v162, v162
	v_fma_f32 v156, v156, s92, 0.5
	v_max_f32_e32 v156, 1.0, v156
	v_cvt_u32_f32_e32 v161, v156
	v_add_f32_e32 v156, 1.0, v160
	v_rcp_f32_e32 v156, v156
	v_mul_f32_e32 v153, 0xbfb8aa3b, v86
	v_mul_f32_e32 v157, 0xbfb8aa3b, v87
	v_exp_f32_e32 v153, v153
	v_fma_f32 v156, v156, s92, 0.5
	v_max_f32_e32 v156, 1.0, v156
	v_cvt_u32_f32_e32 v163, v156
	v_add_f32_e32 v156, 1.0, v162
	v_exp_f32_e32 v157, v157
	v_mul_f32_e32 v160, 0xbfb8aa3b, v88
	v_rcp_f32_e32 v156, v156
	v_mul_f32_e32 v162, 0xbfb8aa3b, v89
	v_exp_f32_e32 v160, v160
	v_exp_f32_e32 v162, v162
	v_mul_f32_e32 v164, 0xbfb8aa3b, v85
	v_exp_f32_e32 v164, v164
	v_add_f32_e32 v153, 1.0, v153
	v_add_f32_e32 v157, 1.0, v157
	v_fma_f32 v156, v156, s92, 0.5
	v_rcp_f32_e32 v153, v153
	v_rcp_f32_e32 v157, v157
	v_add_f32_e32 v160, 1.0, v160
	v_max_f32_e32 v156, 1.0, v156
	v_add_f32_e32 v162, 1.0, v162
	v_rcp_f32_e32 v160, v160
	v_rcp_f32_e32 v162, v162
	v_cvt_u32_f32_sdwa v165, v156 dst_sel:WORD_1 dst_unused:UNUSED_PAD src0_sel:DWORD
	v_add_f32_e32 v156, 1.0, v164
	v_rcp_f32_e32 v156, v156
	v_fma_f32 v153, v153, s92, 0.5
	v_fma_f32 v157, v157, s92, 0.5
	v_max_f32_e32 v153, 1.0, v153
	v_max_f32_e32 v157, 1.0, v157
	v_fma_f32 v160, v160, s92, 0.5
	v_fma_f32 v162, v162, s92, 0.5
	v_cvt_u32_f32_e32 v153, v153
	v_cvt_u32_f32_e32 v157, v157
	v_max_f32_e32 v160, 1.0, v160
	v_max_f32_e32 v162, 1.0, v162
	v_fma_f32 v156, v156, s92, 0.5
	v_cvt_u32_f32_sdwa v160, v160 dst_sel:WORD_1 dst_unused:UNUSED_PAD src0_sel:DWORD
	v_cvt_u32_f32_sdwa v162, v162 dst_sel:BYTE_3 dst_unused:UNUSED_PAD src0_sel:DWORD
	v_max_f32_e32 v156, 1.0, v156
	v_cvt_u32_f32_sdwa v164, v156 dst_sel:BYTE_3 dst_unused:UNUSED_PAD src0_sel:DWORD
	v_lshl_or_b32 v153, v157, 8, v153
	v_mad_i64_i32 v[158:159], s[4:5], v151, s79, v[142:143]
	v_or3_b32 v156, v153, v160, v162
	v_lshl_or_b32 v153, v163, 8, v161
	v_mul_f32_e32 v157, 0xbfb8aa3b, v78
	v_exp_f32_e32 v160, v157
	v_or3_b32 v157, v153, v165, v164
	v_lshl_add_u64 v[158:159], v[158:159], 0, v[140:141]
	global_store_dwordx4 v[158:159], v[154:157], off
	v_add_f32_e32 v153, 1.0, v160
	v_mul_f32_e32 v160, 0xbfb8aa3b, v76
	v_mul_f32_e32 v154, 0xbfb8aa3b, v74
	v_exp_f32_e32 v154, v154
	v_mul_f32_e32 v156, 0xbfb8aa3b, v75
	v_exp_f32_e32 v156, v156
	v_exp_f32_e32 v160, v160
	v_add_f32_e32 v154, 1.0, v154
	v_rcp_f32_e32 v154, v154
	v_mul_f32_e32 v155, 0xbfb8aa3b, v79
	v_exp_f32_e32 v155, v155
	v_mul_f32_e32 v162, 0xbfb8aa3b, v77
	v_fma_f32 v154, v154, s92, 0.5
	v_max_f32_e32 v154, 1.0, v154
	v_cvt_u32_f32_e32 v157, v154
	v_add_f32_e32 v154, 1.0, v156
	v_rcp_f32_e32 v154, v154
	v_mul_f32_e32 v156, 0xbfb8aa3b, v80
	v_exp_f32_e32 v156, v156
	v_add_f32_e32 v155, 1.0, v155
	v_fma_f32 v154, v154, s92, 0.5
	v_max_f32_e32 v154, 1.0, v154
	v_cvt_u32_f32_e32 v161, v154
	v_add_f32_e32 v154, 1.0, v160
	v_mul_f32_e32 v160, 0xbfb8aa3b, v81
	v_exp_f32_e32 v160, v160
	v_rcp_f32_e32 v154, v154
	v_rcp_f32_e32 v153, v153
	v_rcp_f32_e32 v155, v155
	v_add_f32_e32 v156, 1.0, v156
	v_exp_f32_e32 v162, v162
	v_add_f32_e32 v160, 1.0, v160
	v_rcp_f32_e32 v156, v156
	v_rcp_f32_e32 v160, v160
	v_fma_f32 v154, v154, s92, 0.5
	v_max_f32_e32 v154, 1.0, v154
	v_fma_f32 v153, v153, s92, 0.5
	v_fma_f32 v155, v155, s92, 0.5
	v_cvt_u32_f32_sdwa v163, v154 dst_sel:WORD_1 dst_unused:UNUSED_PAD src0_sel:DWORD
	v_add_f32_e32 v154, 1.0, v162
	v_max_f32_e32 v153, 1.0, v153
	v_max_f32_e32 v155, 1.0, v155
	v_fma_f32 v156, v156, s92, 0.5
	v_rcp_f32_e32 v154, v154
	v_fma_f32 v160, v160, s92, 0.5
	v_cvt_u32_f32_e32 v153, v153
	v_cvt_u32_f32_e32 v155, v155
	v_max_f32_e32 v156, 1.0, v156
	v_max_f32_e32 v160, 1.0, v160
	v_cvt_u32_f32_sdwa v156, v156 dst_sel:WORD_1 dst_unused:UNUSED_PAD src0_sel:DWORD
	v_cvt_u32_f32_sdwa v160, v160 dst_sel:BYTE_3 dst_unused:UNUSED_PAD src0_sel:DWORD
	v_fma_f32 v154, v154, s92, 0.5
	v_max_f32_e32 v154, 1.0, v154
	v_lshl_or_b32 v153, v155, 8, v153
	v_cvt_u32_f32_sdwa v162, v154 dst_sel:BYTE_3 dst_unused:UNUSED_PAD src0_sel:DWORD
	v_or3_b32 v154, v153, v156, v160
	v_mul_f32_e32 v156, 0xbfb8aa3b, v66
	v_exp_f32_e32 v156, v156
	v_mul_f32_e32 v160, 0xbfb8aa3b, v67
	v_exp_f32_e32 v160, v160
	v_lshl_or_b32 v155, v161, 8, v157
	v_add_f32_e32 v156, 1.0, v156
	v_rcp_f32_e32 v156, v156
	v_or3_b32 v155, v155, v163, v162
	v_mul_f32_e32 v162, 0xbfb8aa3b, v68
	v_exp_f32_e32 v162, v162
	v_fma_f32 v156, v156, s92, 0.5
	v_max_f32_e32 v156, 1.0, v156
	v_cvt_u32_f32_e32 v161, v156
	v_add_f32_e32 v156, 1.0, v160
	v_rcp_f32_e32 v156, v156
	v_mul_f32_e32 v153, 0xbfb8aa3b, v70
	v_mul_f32_e32 v157, 0xbfb8aa3b, v71
	v_exp_f32_e32 v153, v153
	v_fma_f32 v156, v156, s92, 0.5
	v_max_f32_e32 v156, 1.0, v156
	v_cvt_u32_f32_e32 v163, v156
	v_add_f32_e32 v156, 1.0, v162
	v_exp_f32_e32 v157, v157
	v_mul_f32_e32 v160, 0xbfb8aa3b, v72
	v_rcp_f32_e32 v156, v156
	v_mul_f32_e32 v162, 0xbfb8aa3b, v73
	v_exp_f32_e32 v160, v160
	v_exp_f32_e32 v162, v162
	v_mul_f32_e32 v164, 0xbfb8aa3b, v69
	v_exp_f32_e32 v164, v164
	v_add_f32_e32 v153, 1.0, v153
	v_add_f32_e32 v157, 1.0, v157
	v_fma_f32 v156, v156, s92, 0.5
	v_rcp_f32_e32 v153, v153
	v_rcp_f32_e32 v157, v157
	v_add_f32_e32 v160, 1.0, v160
	v_max_f32_e32 v156, 1.0, v156
	v_add_f32_e32 v162, 1.0, v162
	v_rcp_f32_e32 v160, v160
	v_rcp_f32_e32 v162, v162
	v_cvt_u32_f32_sdwa v165, v156 dst_sel:WORD_1 dst_unused:UNUSED_PAD src0_sel:DWORD
	v_add_f32_e32 v156, 1.0, v164
	v_rcp_f32_e32 v156, v156
	v_fma_f32 v153, v153, s92, 0.5
	v_fma_f32 v157, v157, s92, 0.5
	v_max_f32_e32 v153, 1.0, v153
	v_max_f32_e32 v157, 1.0, v157
	v_fma_f32 v160, v160, s92, 0.5
	v_fma_f32 v162, v162, s92, 0.5
	v_cvt_u32_f32_e32 v153, v153
	v_cvt_u32_f32_e32 v157, v157
	v_max_f32_e32 v160, 1.0, v160
	v_max_f32_e32 v162, 1.0, v162
	v_fma_f32 v156, v156, s92, 0.5
	v_cvt_u32_f32_sdwa v160, v160 dst_sel:WORD_1 dst_unused:UNUSED_PAD src0_sel:DWORD
	v_cvt_u32_f32_sdwa v162, v162 dst_sel:BYTE_3 dst_unused:UNUSED_PAD src0_sel:DWORD
	v_max_f32_e32 v156, 1.0, v156
	v_cvt_u32_f32_sdwa v164, v156 dst_sel:BYTE_3 dst_unused:UNUSED_PAD src0_sel:DWORD
	v_lshl_or_b32 v153, v157, 8, v153
	v_mad_i64_i32 v[158:159], s[4:5], v150, s79, v[142:143]
	v_or3_b32 v156, v153, v160, v162
	v_lshl_or_b32 v153, v163, 8, v161
	v_or3_b32 v157, v153, v165, v164
	v_lshl_add_u64 v[158:159], v[158:159], 0, v[140:141]
	global_store_dwordx4 v[158:159], v[154:157], off
	v_mul_f32_e32 v160, 0xbfb8aa3b, v60
	v_exp_f32_e32 v160, v160
	v_mul_f32_e32 v155, 0xbfb8aa3b, v58
	v_exp_f32_e32 v155, v155
	v_add_u32_e32 v154, 0x80, v149
	v_mad_i64_i32 v[158:159], s[4:5], v154, s79, v[142:143]
	v_add_f32_e32 v154, 1.0, v155
	v_rcp_f32_e32 v154, v154
	v_mul_f32_e32 v156, 0xbfb8aa3b, v59
	v_exp_f32_e32 v156, v156
	v_mul_f32_e32 v153, 0xbfb8aa3b, v62
	v_fma_f32 v154, v154, s92, 0.5
	v_max_f32_e32 v154, 1.0, v154
	v_cvt_u32_f32_e32 v157, v154
	v_add_f32_e32 v154, 1.0, v156
	v_rcp_f32_e32 v154, v154
	v_mul_f32_e32 v155, 0xbfb8aa3b, v63
	v_exp_f32_e32 v153, v153
	v_exp_f32_e32 v155, v155
	v_fma_f32 v154, v154, s92, 0.5
	v_max_f32_e32 v154, 1.0, v154
	v_mul_f32_e32 v156, 0xbfb8aa3b, v64
	v_cvt_u32_f32_e32 v161, v154
	v_add_f32_e32 v154, 1.0, v160
	v_mul_f32_e32 v160, 0xbfb8aa3b, v65
	v_exp_f32_e32 v156, v156
	v_exp_f32_e32 v160, v160
	v_rcp_f32_e32 v154, v154
	v_add_f32_e32 v153, 1.0, v153
	v_add_f32_e32 v155, 1.0, v155
	v_mul_f32_e32 v162, 0xbfb8aa3b, v61
	v_rcp_f32_e32 v153, v153
	v_rcp_f32_e32 v155, v155
	v_add_f32_e32 v156, 1.0, v156
	v_exp_f32_e32 v162, v162
	v_add_f32_e32 v160, 1.0, v160
	v_rcp_f32_e32 v156, v156
	v_rcp_f32_e32 v160, v160
	v_fma_f32 v154, v154, s92, 0.5
	v_max_f32_e32 v154, 1.0, v154
	v_fma_f32 v153, v153, s92, 0.5
	v_fma_f32 v155, v155, s92, 0.5
	v_cvt_u32_f32_sdwa v163, v154 dst_sel:WORD_1 dst_unused:UNUSED_PAD src0_sel:DWORD
	v_add_f32_e32 v154, 1.0, v162
	v_max_f32_e32 v153, 1.0, v153
	v_max_f32_e32 v155, 1.0, v155
	v_fma_f32 v156, v156, s92, 0.5
	v_rcp_f32_e32 v154, v154
	v_fma_f32 v160, v160, s92, 0.5
	v_cvt_u32_f32_e32 v153, v153
	v_cvt_u32_f32_e32 v155, v155
	v_max_f32_e32 v156, 1.0, v156
	v_max_f32_e32 v160, 1.0, v160
	v_cvt_u32_f32_sdwa v156, v156 dst_sel:WORD_1 dst_unused:UNUSED_PAD src0_sel:DWORD
	v_cvt_u32_f32_sdwa v160, v160 dst_sel:BYTE_3 dst_unused:UNUSED_PAD src0_sel:DWORD
	v_fma_f32 v154, v154, s92, 0.5
	v_max_f32_e32 v154, 1.0, v154
	v_lshl_or_b32 v153, v155, 8, v153
	v_cvt_u32_f32_sdwa v162, v154 dst_sel:BYTE_3 dst_unused:UNUSED_PAD src0_sel:DWORD
	v_or3_b32 v154, v153, v156, v160
	v_mul_f32_e32 v156, 0xbfb8aa3b, v50
	v_exp_f32_e32 v156, v156
	v_mul_f32_e32 v160, 0xbfb8aa3b, v51
	v_exp_f32_e32 v160, v160
	v_lshl_or_b32 v155, v161, 8, v157
	v_add_f32_e32 v156, 1.0, v156
	v_rcp_f32_e32 v156, v156
	v_or3_b32 v155, v155, v163, v162
	v_mul_f32_e32 v162, 0xbfb8aa3b, v52
	v_exp_f32_e32 v162, v162
	v_fma_f32 v156, v156, s92, 0.5
	v_max_f32_e32 v156, 1.0, v156
	v_cvt_u32_f32_e32 v161, v156
	v_add_f32_e32 v156, 1.0, v160
	v_rcp_f32_e32 v156, v156
	v_mul_f32_e32 v153, 0xbfb8aa3b, v54
	v_mul_f32_e32 v157, 0xbfb8aa3b, v55
	v_exp_f32_e32 v153, v153
	v_fma_f32 v156, v156, s92, 0.5
	v_max_f32_e32 v156, 1.0, v156
	v_cvt_u32_f32_e32 v163, v156
	v_add_f32_e32 v156, 1.0, v162
	v_exp_f32_e32 v157, v157
	v_mul_f32_e32 v160, 0xbfb8aa3b, v56
	v_rcp_f32_e32 v156, v156
	v_mul_f32_e32 v162, 0xbfb8aa3b, v57
	v_exp_f32_e32 v160, v160
	v_exp_f32_e32 v162, v162
	v_mul_f32_e32 v164, 0xbfb8aa3b, v53
	v_exp_f32_e32 v164, v164
	v_add_f32_e32 v153, 1.0, v153
	v_add_f32_e32 v157, 1.0, v157
	v_fma_f32 v156, v156, s92, 0.5
	v_rcp_f32_e32 v153, v153
	v_rcp_f32_e32 v157, v157
	v_add_f32_e32 v160, 1.0, v160
	v_max_f32_e32 v156, 1.0, v156
	v_add_f32_e32 v162, 1.0, v162
	v_rcp_f32_e32 v160, v160
	v_rcp_f32_e32 v162, v162
	v_cvt_u32_f32_sdwa v165, v156 dst_sel:WORD_1 dst_unused:UNUSED_PAD src0_sel:DWORD
	v_add_f32_e32 v156, 1.0, v164
	v_rcp_f32_e32 v156, v156
	v_fma_f32 v153, v153, s92, 0.5
	v_fma_f32 v157, v157, s92, 0.5
	v_max_f32_e32 v153, 1.0, v153
	v_max_f32_e32 v157, 1.0, v157
	v_fma_f32 v160, v160, s92, 0.5
	v_fma_f32 v162, v162, s92, 0.5
	v_cvt_u32_f32_e32 v153, v153
	v_cvt_u32_f32_e32 v157, v157
	v_max_f32_e32 v160, 1.0, v160
	v_max_f32_e32 v162, 1.0, v162
	v_fma_f32 v156, v156, s92, 0.5
	v_cvt_u32_f32_sdwa v160, v160 dst_sel:WORD_1 dst_unused:UNUSED_PAD src0_sel:DWORD
	v_cvt_u32_f32_sdwa v162, v162 dst_sel:BYTE_3 dst_unused:UNUSED_PAD src0_sel:DWORD
	v_max_f32_e32 v156, 1.0, v156
	v_cvt_u32_f32_sdwa v164, v156 dst_sel:BYTE_3 dst_unused:UNUSED_PAD src0_sel:DWORD
	v_lshl_or_b32 v153, v157, 8, v153
	v_or3_b32 v156, v153, v160, v162
	v_lshl_or_b32 v153, v163, 8, v161
	v_or3_b32 v157, v153, v165, v164
	v_lshl_add_u64 v[158:159], v[158:159], 0, v[140:141]
	global_store_dwordx4 v[158:159], v[154:157], off
	v_mul_f32_e32 v160, 0xbfb8aa3b, v44
	v_exp_f32_e32 v160, v160
	v_mul_f32_e32 v155, 0xbfb8aa3b, v42
	v_exp_f32_e32 v155, v155
	v_add_u32_e32 v154, 0x90, v149
	v_mad_i64_i32 v[158:159], s[4:5], v154, s79, v[142:143]
	v_add_f32_e32 v154, 1.0, v155
	v_rcp_f32_e32 v154, v154
	v_mul_f32_e32 v156, 0xbfb8aa3b, v43
	v_exp_f32_e32 v156, v156
	v_mul_f32_e32 v153, 0xbfb8aa3b, v46
	v_fma_f32 v154, v154, s92, 0.5
	v_max_f32_e32 v154, 1.0, v154
	v_cvt_u32_f32_e32 v157, v154
	v_add_f32_e32 v154, 1.0, v156
	v_rcp_f32_e32 v154, v154
	v_mul_f32_e32 v155, 0xbfb8aa3b, v47
	v_exp_f32_e32 v153, v153
	v_exp_f32_e32 v155, v155
	v_fma_f32 v154, v154, s92, 0.5
	v_max_f32_e32 v154, 1.0, v154
	v_mul_f32_e32 v156, 0xbfb8aa3b, v48
	v_cvt_u32_f32_e32 v161, v154
	v_add_f32_e32 v154, 1.0, v160
	v_mul_f32_e32 v160, 0xbfb8aa3b, v49
	v_exp_f32_e32 v156, v156
	v_exp_f32_e32 v160, v160
	v_rcp_f32_e32 v154, v154
	v_add_f32_e32 v153, 1.0, v153
	v_add_f32_e32 v155, 1.0, v155
	v_mul_f32_e32 v162, 0xbfb8aa3b, v45
	v_rcp_f32_e32 v153, v153
	v_rcp_f32_e32 v155, v155
	v_add_f32_e32 v156, 1.0, v156
	v_exp_f32_e32 v162, v162
	v_add_f32_e32 v160, 1.0, v160
	v_rcp_f32_e32 v156, v156
	v_rcp_f32_e32 v160, v160
	v_fma_f32 v154, v154, s92, 0.5
	v_max_f32_e32 v154, 1.0, v154
	v_fma_f32 v153, v153, s92, 0.5
	v_fma_f32 v155, v155, s92, 0.5
	v_cvt_u32_f32_sdwa v163, v154 dst_sel:WORD_1 dst_unused:UNUSED_PAD src0_sel:DWORD
	v_add_f32_e32 v154, 1.0, v162
	v_max_f32_e32 v153, 1.0, v153
	v_max_f32_e32 v155, 1.0, v155
	v_fma_f32 v156, v156, s92, 0.5
	v_rcp_f32_e32 v154, v154
	v_fma_f32 v160, v160, s92, 0.5
	v_cvt_u32_f32_e32 v153, v153
	v_cvt_u32_f32_e32 v155, v155
	v_max_f32_e32 v156, 1.0, v156
	v_max_f32_e32 v160, 1.0, v160
	v_cvt_u32_f32_sdwa v156, v156 dst_sel:WORD_1 dst_unused:UNUSED_PAD src0_sel:DWORD
	v_cvt_u32_f32_sdwa v160, v160 dst_sel:BYTE_3 dst_unused:UNUSED_PAD src0_sel:DWORD
	v_fma_f32 v154, v154, s92, 0.5
	v_max_f32_e32 v154, 1.0, v154
	v_lshl_or_b32 v153, v155, 8, v153
	v_cvt_u32_f32_sdwa v162, v154 dst_sel:BYTE_3 dst_unused:UNUSED_PAD src0_sel:DWORD
	v_or3_b32 v154, v153, v156, v160
	v_mul_f32_e32 v156, 0xbfb8aa3b, v34
	v_exp_f32_e32 v156, v156
	v_mul_f32_e32 v160, 0xbfb8aa3b, v35
	v_exp_f32_e32 v160, v160
	v_lshl_or_b32 v155, v161, 8, v157
	v_add_f32_e32 v156, 1.0, v156
	v_rcp_f32_e32 v156, v156
	v_or3_b32 v155, v155, v163, v162
	v_mul_f32_e32 v162, 0xbfb8aa3b, v36
	v_exp_f32_e32 v162, v162
	v_fma_f32 v156, v156, s92, 0.5
	v_max_f32_e32 v156, 1.0, v156
	v_cvt_u32_f32_e32 v161, v156
	v_add_f32_e32 v156, 1.0, v160
	v_rcp_f32_e32 v156, v156
	v_mul_f32_e32 v153, 0xbfb8aa3b, v38
	v_mul_f32_e32 v157, 0xbfb8aa3b, v39
	v_exp_f32_e32 v153, v153
	v_fma_f32 v156, v156, s92, 0.5
	v_max_f32_e32 v156, 1.0, v156
	v_cvt_u32_f32_e32 v163, v156
	v_add_f32_e32 v156, 1.0, v162
	v_exp_f32_e32 v157, v157
	v_mul_f32_e32 v160, 0xbfb8aa3b, v40
	v_rcp_f32_e32 v156, v156
	v_mul_f32_e32 v162, 0xbfb8aa3b, v41
	v_exp_f32_e32 v160, v160
	v_exp_f32_e32 v162, v162
	v_mul_f32_e32 v164, 0xbfb8aa3b, v37
	v_exp_f32_e32 v164, v164
	v_add_f32_e32 v153, 1.0, v153
	v_add_f32_e32 v157, 1.0, v157
	v_fma_f32 v156, v156, s92, 0.5
	v_rcp_f32_e32 v153, v153
	v_rcp_f32_e32 v157, v157
	v_add_f32_e32 v160, 1.0, v160
	v_max_f32_e32 v156, 1.0, v156
	v_add_f32_e32 v162, 1.0, v162
	v_rcp_f32_e32 v160, v160
	v_rcp_f32_e32 v162, v162
	v_cvt_u32_f32_sdwa v165, v156 dst_sel:WORD_1 dst_unused:UNUSED_PAD src0_sel:DWORD
	v_add_f32_e32 v156, 1.0, v164
	v_rcp_f32_e32 v156, v156
	v_fma_f32 v153, v153, s92, 0.5
	v_fma_f32 v157, v157, s92, 0.5
	v_max_f32_e32 v153, 1.0, v153
	v_max_f32_e32 v157, 1.0, v157
	v_fma_f32 v160, v160, s92, 0.5
	v_fma_f32 v162, v162, s92, 0.5
	v_cvt_u32_f32_e32 v153, v153
	v_cvt_u32_f32_e32 v157, v157
	v_max_f32_e32 v160, 1.0, v160
	v_max_f32_e32 v162, 1.0, v162
	v_fma_f32 v156, v156, s92, 0.5
	v_cvt_u32_f32_sdwa v160, v160 dst_sel:WORD_1 dst_unused:UNUSED_PAD src0_sel:DWORD
	v_cvt_u32_f32_sdwa v162, v162 dst_sel:BYTE_3 dst_unused:UNUSED_PAD src0_sel:DWORD
	v_max_f32_e32 v156, 1.0, v156
	v_cvt_u32_f32_sdwa v164, v156 dst_sel:BYTE_3 dst_unused:UNUSED_PAD src0_sel:DWORD
	v_lshl_or_b32 v153, v157, 8, v153
	v_or3_b32 v156, v153, v160, v162
	v_lshl_or_b32 v153, v163, 8, v161
	v_or3_b32 v157, v153, v165, v164
	v_lshl_add_u64 v[158:159], v[158:159], 0, v[140:141]
	global_store_dwordx4 v[158:159], v[154:157], off
	v_mul_f32_e32 v160, 0xbfb8aa3b, v28
	v_exp_f32_e32 v160, v160
	v_mul_f32_e32 v155, 0xbfb8aa3b, v26
	v_exp_f32_e32 v155, v155
	v_add_u32_e32 v154, 0xa0, v149
	v_mad_i64_i32 v[158:159], s[4:5], v154, s79, v[142:143]
	v_add_f32_e32 v154, 1.0, v155
	v_rcp_f32_e32 v154, v154
	v_mul_f32_e32 v156, 0xbfb8aa3b, v27
	v_exp_f32_e32 v156, v156
	v_mul_f32_e32 v153, 0xbfb8aa3b, v30
	v_fma_f32 v154, v154, s92, 0.5
	v_max_f32_e32 v154, 1.0, v154
	v_cvt_u32_f32_e32 v157, v154
	v_add_f32_e32 v154, 1.0, v156
	v_rcp_f32_e32 v154, v154
	v_mul_f32_e32 v155, 0xbfb8aa3b, v31
	v_exp_f32_e32 v153, v153
	v_exp_f32_e32 v155, v155
	v_fma_f32 v154, v154, s92, 0.5
	v_max_f32_e32 v154, 1.0, v154
	v_mul_f32_e32 v156, 0xbfb8aa3b, v32
	v_cvt_u32_f32_e32 v161, v154
	v_add_f32_e32 v154, 1.0, v160
	v_mul_f32_e32 v160, 0xbfb8aa3b, v33
	v_exp_f32_e32 v156, v156
	v_exp_f32_e32 v160, v160
	v_rcp_f32_e32 v154, v154
	v_add_f32_e32 v153, 1.0, v153
	v_add_f32_e32 v155, 1.0, v155
	v_mul_f32_e32 v162, 0xbfb8aa3b, v29
	v_rcp_f32_e32 v153, v153
	v_rcp_f32_e32 v155, v155
	v_add_f32_e32 v156, 1.0, v156
	v_exp_f32_e32 v162, v162
	v_add_f32_e32 v160, 1.0, v160
	v_rcp_f32_e32 v156, v156
	v_rcp_f32_e32 v160, v160
	v_fma_f32 v154, v154, s92, 0.5
	v_max_f32_e32 v154, 1.0, v154
	v_fma_f32 v153, v153, s92, 0.5
	v_fma_f32 v155, v155, s92, 0.5
	v_cvt_u32_f32_sdwa v163, v154 dst_sel:WORD_1 dst_unused:UNUSED_PAD src0_sel:DWORD
	v_add_f32_e32 v154, 1.0, v162
	v_max_f32_e32 v153, 1.0, v153
	v_max_f32_e32 v155, 1.0, v155
	v_fma_f32 v156, v156, s92, 0.5
	v_rcp_f32_e32 v154, v154
	v_fma_f32 v160, v160, s92, 0.5
	v_cvt_u32_f32_e32 v153, v153
	v_cvt_u32_f32_e32 v155, v155
	v_max_f32_e32 v156, 1.0, v156
	v_max_f32_e32 v160, 1.0, v160
	v_cvt_u32_f32_sdwa v156, v156 dst_sel:WORD_1 dst_unused:UNUSED_PAD src0_sel:DWORD
	v_cvt_u32_f32_sdwa v160, v160 dst_sel:BYTE_3 dst_unused:UNUSED_PAD src0_sel:DWORD
	v_fma_f32 v154, v154, s92, 0.5
	v_max_f32_e32 v154, 1.0, v154
	v_lshl_or_b32 v153, v155, 8, v153
	v_cvt_u32_f32_sdwa v162, v154 dst_sel:BYTE_3 dst_unused:UNUSED_PAD src0_sel:DWORD
	v_or3_b32 v154, v153, v156, v160
	v_mul_f32_e32 v156, 0xbfb8aa3b, v18
	v_exp_f32_e32 v156, v156
	v_mul_f32_e32 v160, 0xbfb8aa3b, v19
	v_exp_f32_e32 v160, v160
	v_lshl_or_b32 v155, v161, 8, v157
	v_add_f32_e32 v156, 1.0, v156
	v_rcp_f32_e32 v156, v156
	v_or3_b32 v155, v155, v163, v162
	v_mul_f32_e32 v162, 0xbfb8aa3b, v20
	v_exp_f32_e32 v162, v162
	v_fma_f32 v156, v156, s92, 0.5
	v_max_f32_e32 v156, 1.0, v156
	v_cvt_u32_f32_e32 v161, v156
	v_add_f32_e32 v156, 1.0, v160
	v_rcp_f32_e32 v156, v156
	v_mul_f32_e32 v153, 0xbfb8aa3b, v22
	v_mul_f32_e32 v157, 0xbfb8aa3b, v23
	v_exp_f32_e32 v153, v153
	v_fma_f32 v156, v156, s92, 0.5
	v_max_f32_e32 v156, 1.0, v156
	v_cvt_u32_f32_e32 v163, v156
	v_add_f32_e32 v156, 1.0, v162
	v_exp_f32_e32 v157, v157
	v_mul_f32_e32 v160, 0xbfb8aa3b, v24
	v_rcp_f32_e32 v156, v156
	v_mul_f32_e32 v162, 0xbfb8aa3b, v25
	v_exp_f32_e32 v160, v160
	v_exp_f32_e32 v162, v162
	v_mul_f32_e32 v164, 0xbfb8aa3b, v21
	v_exp_f32_e32 v164, v164
	v_add_f32_e32 v153, 1.0, v153
	v_add_f32_e32 v157, 1.0, v157
	v_fma_f32 v156, v156, s92, 0.5
	v_rcp_f32_e32 v153, v153
	v_rcp_f32_e32 v157, v157
	v_add_f32_e32 v160, 1.0, v160
	v_max_f32_e32 v156, 1.0, v156
	v_add_f32_e32 v162, 1.0, v162
	v_rcp_f32_e32 v160, v160
	v_rcp_f32_e32 v162, v162
	v_cvt_u32_f32_sdwa v165, v156 dst_sel:WORD_1 dst_unused:UNUSED_PAD src0_sel:DWORD
	v_add_f32_e32 v156, 1.0, v164
	v_rcp_f32_e32 v156, v156
	v_fma_f32 v153, v153, s92, 0.5
	v_fma_f32 v157, v157, s92, 0.5
	v_max_f32_e32 v153, 1.0, v153
	v_max_f32_e32 v157, 1.0, v157
	v_fma_f32 v160, v160, s92, 0.5
	v_fma_f32 v162, v162, s92, 0.5
	v_cvt_u32_f32_e32 v153, v153
	v_cvt_u32_f32_e32 v157, v157
	v_max_f32_e32 v160, 1.0, v160
	v_max_f32_e32 v162, 1.0, v162
	v_fma_f32 v156, v156, s92, 0.5
	v_cvt_u32_f32_sdwa v160, v160 dst_sel:WORD_1 dst_unused:UNUSED_PAD src0_sel:DWORD
	v_cvt_u32_f32_sdwa v162, v162 dst_sel:BYTE_3 dst_unused:UNUSED_PAD src0_sel:DWORD
	v_max_f32_e32 v156, 1.0, v156
	v_cvt_u32_f32_sdwa v164, v156 dst_sel:BYTE_3 dst_unused:UNUSED_PAD src0_sel:DWORD
	v_lshl_or_b32 v153, v157, 8, v153
	v_or3_b32 v156, v153, v160, v162
	v_lshl_or_b32 v153, v163, 8, v161
	v_or3_b32 v157, v153, v165, v164
	v_lshl_add_u64 v[158:159], v[158:159], 0, v[140:141]
	global_store_dwordx4 v[158:159], v[154:157], off
	v_mul_f32_e32 v158, 0xbfb8aa3b, v12
	v_exp_f32_e32 v158, v158
	v_mul_f32_e32 v155, 0xbfb8aa3b, v10
	v_exp_f32_e32 v155, v155
	v_add_u32_e32 v154, 0xb0, v149
	v_mad_i64_i32 v[142:143], s[4:5], v154, s79, v[142:143]
	v_add_f32_e32 v154, 1.0, v155
	v_rcp_f32_e32 v154, v154
	v_mul_f32_e32 v156, 0xbfb8aa3b, v11
	v_exp_f32_e32 v156, v156
	v_mul_f32_e32 v153, 0xbfb8aa3b, v14
	v_fma_f32 v154, v154, s92, 0.5
	v_max_f32_e32 v154, 1.0, v154
	v_cvt_u32_f32_e32 v157, v154
	v_add_f32_e32 v154, 1.0, v156
	v_rcp_f32_e32 v154, v154
	v_mul_f32_e32 v155, 0xbfb8aa3b, v15
	v_exp_f32_e32 v153, v153
	v_exp_f32_e32 v155, v155
	v_fma_f32 v154, v154, s92, 0.5
	v_max_f32_e32 v154, 1.0, v154
	v_mul_f32_e32 v156, 0xbfb8aa3b, v16
	v_cvt_u32_f32_e32 v159, v154
	v_add_f32_e32 v154, 1.0, v158
	v_mul_f32_e32 v158, 0xbfb8aa3b, v17
	v_exp_f32_e32 v156, v156
	v_exp_f32_e32 v158, v158
	v_rcp_f32_e32 v154, v154
	v_add_f32_e32 v153, 1.0, v153
	v_add_f32_e32 v155, 1.0, v155
	v_mul_f32_e32 v160, 0xbfb8aa3b, v13
	v_rcp_f32_e32 v153, v153
	v_rcp_f32_e32 v155, v155
	v_add_f32_e32 v156, 1.0, v156
	v_exp_f32_e32 v160, v160
	v_add_f32_e32 v158, 1.0, v158
	v_rcp_f32_e32 v156, v156
	v_rcp_f32_e32 v158, v158
	v_fma_f32 v154, v154, s92, 0.5
	v_max_f32_e32 v154, 1.0, v154
	v_fma_f32 v153, v153, s92, 0.5
	v_fma_f32 v155, v155, s92, 0.5
	v_cvt_u32_f32_sdwa v161, v154 dst_sel:WORD_1 dst_unused:UNUSED_PAD src0_sel:DWORD
	v_add_f32_e32 v154, 1.0, v160
	v_max_f32_e32 v153, 1.0, v153
	v_max_f32_e32 v155, 1.0, v155
	v_fma_f32 v156, v156, s92, 0.5
	v_rcp_f32_e32 v154, v154
	v_fma_f32 v158, v158, s92, 0.5
	v_cvt_u32_f32_e32 v153, v153
	v_cvt_u32_f32_e32 v155, v155
	v_max_f32_e32 v156, 1.0, v156
	v_max_f32_e32 v158, 1.0, v158
	v_cvt_u32_f32_sdwa v156, v156 dst_sel:WORD_1 dst_unused:UNUSED_PAD src0_sel:DWORD
	v_cvt_u32_f32_sdwa v158, v158 dst_sel:BYTE_3 dst_unused:UNUSED_PAD src0_sel:DWORD
	v_fma_f32 v154, v154, s92, 0.5
	v_max_f32_e32 v154, 1.0, v154
	v_lshl_or_b32 v153, v155, 8, v153
	v_cvt_u32_f32_sdwa v160, v154 dst_sel:BYTE_3 dst_unused:UNUSED_PAD src0_sel:DWORD
	v_or3_b32 v154, v153, v156, v158
	v_mul_f32_e32 v156, 0xbfb8aa3b, v2
	v_exp_f32_e32 v156, v156
	v_mul_f32_e32 v158, 0xbfb8aa3b, v3
	v_exp_f32_e32 v158, v158
	v_lshl_or_b32 v155, v159, 8, v157
	v_add_f32_e32 v156, 1.0, v156
	v_rcp_f32_e32 v156, v156
	v_or3_b32 v155, v155, v161, v160
	v_mul_f32_e32 v160, 0xbfb8aa3b, v4
	v_exp_f32_e32 v160, v160
	v_fma_f32 v156, v156, s92, 0.5
	v_max_f32_e32 v156, 1.0, v156
	v_cvt_u32_f32_e32 v159, v156
	v_add_f32_e32 v156, 1.0, v158
	v_rcp_f32_e32 v156, v156
	v_mul_f32_e32 v153, 0xbfb8aa3b, v6
	v_mul_f32_e32 v157, 0xbfb8aa3b, v7
	v_exp_f32_e32 v153, v153
	v_fma_f32 v156, v156, s92, 0.5
	v_max_f32_e32 v156, 1.0, v156
	v_cvt_u32_f32_e32 v161, v156
	v_add_f32_e32 v156, 1.0, v160
	v_exp_f32_e32 v157, v157
	v_mul_f32_e32 v158, 0xbfb8aa3b, v8
	v_rcp_f32_e32 v156, v156
	v_mul_f32_e32 v160, 0xbfb8aa3b, v9
	v_exp_f32_e32 v158, v158
	v_exp_f32_e32 v160, v160
	v_mul_f32_e32 v162, 0xbfb8aa3b, v5
	v_exp_f32_e32 v162, v162
	v_add_f32_e32 v153, 1.0, v153
	v_add_f32_e32 v157, 1.0, v157
	v_fma_f32 v156, v156, s92, 0.5
	v_rcp_f32_e32 v153, v153
	v_rcp_f32_e32 v157, v157
	v_add_f32_e32 v158, 1.0, v158
	v_max_f32_e32 v156, 1.0, v156
	v_add_f32_e32 v160, 1.0, v160
	v_rcp_f32_e32 v158, v158
	v_rcp_f32_e32 v160, v160
	v_cvt_u32_f32_sdwa v163, v156 dst_sel:WORD_1 dst_unused:UNUSED_PAD src0_sel:DWORD
	v_add_f32_e32 v156, 1.0, v162
	v_rcp_f32_e32 v156, v156
	v_fma_f32 v153, v153, s92, 0.5
	v_fma_f32 v157, v157, s92, 0.5
	v_max_f32_e32 v153, 1.0, v153
	v_max_f32_e32 v157, 1.0, v157
	v_fma_f32 v158, v158, s92, 0.5
	v_fma_f32 v160, v160, s92, 0.5
	v_cvt_u32_f32_e32 v153, v153
	v_cvt_u32_f32_e32 v157, v157
	v_max_f32_e32 v158, 1.0, v158
	v_max_f32_e32 v160, 1.0, v160
	v_fma_f32 v156, v156, s92, 0.5
	v_cvt_u32_f32_sdwa v158, v158 dst_sel:WORD_1 dst_unused:UNUSED_PAD src0_sel:DWORD
	v_cvt_u32_f32_sdwa v160, v160 dst_sel:BYTE_3 dst_unused:UNUSED_PAD src0_sel:DWORD
	v_max_f32_e32 v156, 1.0, v156
	v_cvt_u32_f32_sdwa v162, v156 dst_sel:BYTE_3 dst_unused:UNUSED_PAD src0_sel:DWORD
	v_lshl_or_b32 v153, v157, 8, v153
	v_or3_b32 v156, v153, v158, v160
	v_lshl_or_b32 v153, v161, 8, v159
	v_or3_b32 v157, v153, v163, v162
	v_lshl_add_u64 v[140:141], v[142:143], 0, v[140:141]
	global_store_dwordx4 v[140:141], v[154:157], off
	s_mov_b32 s32, 0
	s_cbranch_execnz .LBB0_94
.LBB0_96:
	v_add_u32_e32 v140, s27, v147
	v_ashrrev_i32_e32 v141, 31, v140
	v_mov_b64_e32 v[142:143], s[18:19]
	v_cvt_pk_bf16_f32 v70, v70, v71
	v_cvt_pk_bf16_f32 v71, v72, v73
	v_cvt_pk_bf16_f32 v72, v66, v67
	v_add_u32_e32 v66, 0x80, v149
	v_cvt_pk_bf16_f32 v54, v54, v55
	v_cvt_pk_bf16_f32 v55, v56, v57
	v_cvt_pk_bf16_f32 v56, v50, v51
	v_add_u32_e32 v50, 0x90, v149
	v_cvt_pk_bf16_f32 v38, v38, v39
	v_cvt_pk_bf16_f32 v39, v40, v41
	v_cvt_pk_bf16_f32 v40, v34, v35
	v_add_u32_e32 v34, 0xa0, v149
	v_cvt_pk_bf16_f32 v22, v22, v23
	v_cvt_pk_bf16_f32 v23, v24, v25
	v_cvt_pk_bf16_f32 v24, v18, v19
	v_add_u32_e32 v18, 0xb0, v149
	v_mad_i64_i32 v[154:155], s[4:5], v149, s93, v[142:143]
	v_lshlrev_b64 v[140:141], 1, v[140:141]
	v_cvt_pk_bf16_f32 v118, v118, v119
	v_cvt_pk_bf16_f32 v119, v120, v121
	v_cvt_pk_bf16_f32 v120, v114, v115
	v_mad_i64_i32 v[114:115], s[4:5], v152, s93, v[142:143]
	v_cvt_pk_bf16_f32 v102, v102, v103
	v_cvt_pk_bf16_f32 v103, v104, v105
	v_cvt_pk_bf16_f32 v104, v98, v99
	v_mad_i64_i32 v[98:99], s[4:5], v151, s93, v[142:143]
	v_cvt_pk_bf16_f32 v86, v86, v87
	v_cvt_pk_bf16_f32 v87, v88, v89
	v_cvt_pk_bf16_f32 v88, v82, v83
	v_mad_i64_i32 v[82:83], s[4:5], v150, s93, v[142:143]
	v_mad_i64_i32 v[66:67], s[4:5], v66, s93, v[142:143]
	v_mad_i64_i32 v[50:51], s[4:5], v50, s93, v[142:143]
	v_mad_i64_i32 v[34:35], s[4:5], v34, s93, v[142:143]
	v_mad_i64_i32 v[18:19], s[4:5], v18, s93, v[142:143]
	v_lshl_add_u64 v[154:155], v[154:155], 0, v[140:141]
	v_cvt_pk_bf16_f32 v122, v122, v123
	v_cvt_pk_bf16_f32 v123, v124, v125
	v_cvt_pk_bf16_f32 v124, v126, v127
	v_cvt_pk_bf16_f32 v125, v128, v129
	v_cvt_pk_bf16_f32 v121, v116, v117
	v_lshl_add_u64 v[114:115], v[114:115], 0, v[140:141]
	v_cvt_pk_bf16_f32 v110, v110, v111
	v_cvt_pk_bf16_f32 v111, v112, v113
	v_cvt_pk_bf16_f32 v112, v106, v107
	v_cvt_pk_bf16_f32 v113, v108, v109
	v_cvt_pk_bf16_f32 v105, v100, v101
	v_lshl_add_u64 v[98:99], v[98:99], 0, v[140:141]
	v_cvt_pk_bf16_f32 v94, v94, v95
	v_cvt_pk_bf16_f32 v95, v96, v97
	v_cvt_pk_bf16_f32 v96, v90, v91
	v_cvt_pk_bf16_f32 v97, v92, v93
	v_cvt_pk_bf16_f32 v89, v84, v85
	v_lshl_add_u64 v[82:83], v[82:83], 0, v[140:141]
	v_cvt_pk_bf16_f32 v78, v78, v79
	v_cvt_pk_bf16_f32 v79, v80, v81
	v_cvt_pk_bf16_f32 v80, v74, v75
	v_cvt_pk_bf16_f32 v81, v76, v77
	v_cvt_pk_bf16_f32 v73, v68, v69
	v_lshl_add_u64 v[66:67], v[66:67], 0, v[140:141]
	v_cvt_pk_bf16_f32 v62, v62, v63
	v_cvt_pk_bf16_f32 v63, v64, v65
	v_cvt_pk_bf16_f32 v64, v58, v59
	v_cvt_pk_bf16_f32 v65, v60, v61
	v_cvt_pk_bf16_f32 v57, v52, v53
	v_lshl_add_u64 v[50:51], v[50:51], 0, v[140:141]
	v_cvt_pk_bf16_f32 v46, v46, v47
	v_cvt_pk_bf16_f32 v47, v48, v49
	v_cvt_pk_bf16_f32 v48, v42, v43
	v_cvt_pk_bf16_f32 v49, v44, v45
	v_cvt_pk_bf16_f32 v41, v36, v37
	v_lshl_add_u64 v[34:35], v[34:35], 0, v[140:141]
	v_cvt_pk_bf16_f32 v30, v30, v31
	v_cvt_pk_bf16_f32 v31, v32, v33
	v_cvt_pk_bf16_f32 v32, v26, v27
	v_cvt_pk_bf16_f32 v33, v28, v29
	v_cvt_pk_bf16_f32 v25, v20, v21
	v_lshl_add_u64 v[18:19], v[18:19], 0, v[140:141]
	v_cvt_pk_bf16_f32 v14, v14, v15
	v_cvt_pk_bf16_f32 v15, v16, v17
	v_cvt_pk_bf16_f32 v16, v10, v11
	v_cvt_pk_bf16_f32 v17, v12, v13
	v_cvt_pk_bf16_f32 v6, v6, v7
	v_cvt_pk_bf16_f32 v7, v8, v9
	v_cvt_pk_bf16_f32 v8, v2, v3
	v_cvt_pk_bf16_f32 v9, v4, v5
	global_store_dwordx4 v[154:155], v[122:125], off
	global_store_dwordx4 v[154:155], v[118:121], off offset:256
	global_store_dwordx4 v[114:115], v[110:113], off
	global_store_dwordx4 v[114:115], v[102:105], off offset:256
	global_store_dwordx4 v[98:99], v[94:97], off
	global_store_dwordx4 v[98:99], v[86:89], off offset:256
	global_store_dwordx4 v[82:83], v[78:81], off
	global_store_dwordx4 v[82:83], v[70:73], off offset:256
	global_store_dwordx4 v[66:67], v[62:65], off
	global_store_dwordx4 v[66:67], v[54:57], off offset:256
	global_store_dwordx4 v[50:51], v[46:49], off
	global_store_dwordx4 v[50:51], v[38:41], off offset:256
	global_store_dwordx4 v[34:35], v[30:33], off
	global_store_dwordx4 v[34:35], v[22:25], off offset:256
	global_store_dwordx4 v[18:19], v[14:17], off
	global_store_dwordx4 v[18:19], v[6:9], off offset:256
	s_mov_b32 s32, 1
	s_and_b64 vcc, exec, s[8:9]
	s_mov_b64 s[4:5], -1
	s_cbranch_vccnz .LBB0_82

.LBB0_113:
	s_andn2_b64 vcc, exec, s[14:15]
	s_cbranch_vccnz .LBB0_116
	s_add_u32 s30, s30, 0x80
	s_addc_u32 s31, s31, 0
	s_add_u32 s19, s34, 0x100
	s_addc_u32 s21, s35, 0
	s_mov_b32 s4, 0
	s_add_i32 s34, s4, 2
	s_add_u32 s35, s30, 0x80
	s_addc_u32 s5, s31, 0
	s_add_i32 s58, 0, 0x10000
	s_cmp_eq_u32 s48, s4
	s_cselect_b32 s5, s27, s5
	s_cselect_b32 s4, s26, s35
	s_cselect_b32 s57, s29, s21
	s_cselect_b32 s56, s28, s19
	s_add_i32 s35, 0, 0x14000
	v_add_u32_e32 v156, s58, v141
	v_add_u32_e32 v172, s35, v141
	ds_read_b128 v[144:147], v156
	ds_read_b128 v[148:151], v156 offset:1024
	ds_read_b128 v[152:155], v156 offset:2048
	ds_read_b128 v[156:159], v156 offset:3072
	ds_read_b128 v[160:163], v172
	ds_read_b128 v[164:167], v172 offset:1024
	ds_read_b128 v[168:171], v172 offset:2048
	ds_read_b128 v[172:175], v172 offset:3072
	v_lshl_add_u64 v[196:197], s[30:31], 0, v[136:137]
	s_add_i32 m0, s3, 0xc000
	ds_read_b128 v[176:179], v143
	ds_read_b128 v[180:183], v143 offset:1024
	ds_read_b128 v[184:187], v143 offset:2048
	ds_read_b128 v[188:191], v143 offset:3072
	ds_read_b128 v[192:195], v143 offset:4096
	ds_read_b128 v[202:205], v143 offset:5120
	ds_read_b128 v[206:209], v143 offset:6144
	ds_read_b128 v[210:213], v143 offset:7168
	global_load_lds_dwordx4 v[196:197], off
	v_lshl_add_u64 v[196:197], s[30:31], 0, v[138:139]
	s_add_i32 m0, s3, 0xe000
	s_nop 0
	global_load_lds_dwordx4 v[196:197], off
	s_waitcnt vmcnt(24)
	s_waitcnt lgkmcnt(0)
	s_barrier
	s_setprio 1
	s_waitcnt lgkmcnt(0)
	v_mfma_f32_16x16x32_bf16 v[122:125], v[144:147], v[176:179], 0
	v_mfma_f32_16x16x32_bf16 v[126:129], v[152:155], v[176:179], 0
	v_mfma_f32_16x16x32_bf16 v[110:113], v[144:147], v[184:187], 0
	v_mfma_f32_16x16x32_bf16 v[106:109], v[152:155], v[184:187], 0
	v_mfma_f32_16x16x32_bf16 v[94:97], v[144:147], v[192:195], 0
	v_mfma_f32_16x16x32_bf16 v[90:93], v[152:155], v[192:195], 0
	v_mfma_f32_16x16x32_bf16 v[78:81], v[144:147], v[206:209], 0
	v_mfma_f32_16x16x32_bf16 v[74:77], v[152:155], v[206:209], 0
	v_mfma_f32_16x16x32_bf16 v[122:125], v[148:151], v[180:183], v[122:125]
	v_mfma_f32_16x16x32_bf16 v[126:129], v[156:159], v[180:183], v[126:129]
	v_mfma_f32_16x16x32_bf16 v[110:113], v[148:151], v[188:191], v[110:113]
	v_mfma_f32_16x16x32_bf16 v[106:109], v[156:159], v[188:191], v[106:109]
	v_mfma_f32_16x16x32_bf16 v[94:97], v[148:151], v[202:205], v[94:97]
	v_mfma_f32_16x16x32_bf16 v[90:93], v[156:159], v[202:205], v[90:93]
	v_mfma_f32_16x16x32_bf16 v[78:81], v[148:151], v[210:213], v[78:81]
	v_mfma_f32_16x16x32_bf16 v[74:77], v[156:159], v[210:213], v[74:77]
	s_setprio 0
	s_setprio 1
	v_mfma_f32_16x16x32_bf16 v[118:121], v[160:163], v[176:179], 0
	v_mfma_f32_16x16x32_bf16 v[114:117], v[168:171], v[176:179], 0
	v_mfma_f32_16x16x32_bf16 v[102:105], v[160:163], v[184:187], 0
	v_mfma_f32_16x16x32_bf16 v[98:101], v[168:171], v[184:187], 0
	v_mfma_f32_16x16x32_bf16 v[86:89], v[160:163], v[192:195], 0
	v_mfma_f32_16x16x32_bf16 v[82:85], v[168:171], v[192:195], 0
	v_mfma_f32_16x16x32_bf16 v[70:73], v[160:163], v[206:209], 0
	v_mfma_f32_16x16x32_bf16 v[66:69], v[168:171], v[206:209], 0
	v_mfma_f32_16x16x32_bf16 v[118:121], v[164:167], v[180:183], v[118:121]
	v_mfma_f32_16x16x32_bf16 v[114:117], v[172:175], v[180:183], v[114:117]
	v_mfma_f32_16x16x32_bf16 v[102:105], v[164:167], v[188:191], v[102:105]
	v_mfma_f32_16x16x32_bf16 v[98:101], v[172:175], v[188:191], v[98:101]
	v_mfma_f32_16x16x32_bf16 v[86:89], v[164:167], v[202:205], v[86:89]
	v_mfma_f32_16x16x32_bf16 v[82:85], v[172:175], v[202:205], v[82:85]
	v_mfma_f32_16x16x32_bf16 v[70:73], v[164:167], v[210:213], v[70:73]
	v_mfma_f32_16x16x32_bf16 v[66:69], v[172:175], v[210:213], v[66:69]
	s_setprio 0
	s_barrier
	s_add_i32 s58, s58, s51
	v_lshl_add_u64 v[196:197], s[56:57], 0, v[0:1]
	s_mov_b32 m0, s58
	ds_read_b128 v[176:179], v143 offset:16384
	ds_read_b128 v[180:183], v143 offset:17408
	ds_read_b128 v[184:187], v143 offset:18432
	ds_read_b128 v[188:191], v143 offset:19456
	ds_read_b128 v[192:195], v143 offset:20480
	ds_read_b128 v[202:205], v143 offset:21504
	ds_read_b128 v[206:209], v143 offset:22528
	ds_read_b128 v[210:213], v143 offset:23552
	global_load_lds_dwordx4 v[196:197], off
	s_add_i32 m0, s58, 0x2000
	v_lshl_add_u64 v[214:215], s[56:57], 0, v[130:131]
	s_add_u32 s56, s56, s8
	s_addc_u32 s57, s57, s9
	s_add_i32 s35, s35, s51
	global_load_lds_dwordx4 v[214:215], off
	v_lshl_add_u64 v[216:217], s[56:57], 0, v[0:1]
	s_mov_b32 m0, s35
	v_lshl_add_u64 v[218:219], s[56:57], 0, v[130:131]
	global_load_lds_dwordx4 v[216:217], off
	s_add_i32 m0, s35, 0x2000
	v_lshl_add_u64 v[220:221], s[4:5], 0, v[132:133]
	global_load_lds_dwordx4 v[218:219], off
	s_mov_b32 m0, s3
	v_lshl_add_u64 v[234:235], s[4:5], 0, v[134:135]
	global_load_lds_dwordx4 v[220:221], off
	s_mov_b32 m0, s42
	s_nop 0
	global_load_lds_dwordx4 v[234:235], off
	s_cmp_eq_u32 s49, 1
	s_cbranch_scc1 .Lfw_kv_8
	s_waitcnt vmcnt(24)
	s_branch .Lfw_kv_d
.Lfw_kv_8:
	s_waitcnt vmcnt(8)
.Lfw_kv_d:
	s_waitcnt lgkmcnt(0)
	s_barrier
	s_setprio 1
	s_waitcnt lgkmcnt(0)
	v_mfma_f32_16x16x32_bf16 v[62:65], v[144:147], v[176:179], 0
	v_mfma_f32_16x16x32_bf16 v[58:61], v[152:155], v[176:179], 0
	v_mfma_f32_16x16x32_bf16 v[46:49], v[144:147], v[184:187], 0
	v_mfma_f32_16x16x32_bf16 v[42:45], v[152:155], v[184:187], 0
	v_mfma_f32_16x16x32_bf16 v[30:33], v[144:147], v[192:195], 0
	v_mfma_f32_16x16x32_bf16 v[26:29], v[152:155], v[192:195], 0
	v_mfma_f32_16x16x32_bf16 v[14:17], v[144:147], v[206:209], 0
	v_mfma_f32_16x16x32_bf16 v[10:13], v[152:155], v[206:209], 0
	v_mfma_f32_16x16x32_bf16 v[62:65], v[148:151], v[180:183], v[62:65]
	v_mfma_f32_16x16x32_bf16 v[58:61], v[156:159], v[180:183], v[58:61]
	v_mfma_f32_16x16x32_bf16 v[46:49], v[148:151], v[188:191], v[46:49]
	v_mfma_f32_16x16x32_bf16 v[42:45], v[156:159], v[188:191], v[42:45]
	v_mfma_f32_16x16x32_bf16 v[30:33], v[148:151], v[202:205], v[30:33]
	v_mfma_f32_16x16x32_bf16 v[26:29], v[156:159], v[202:205], v[26:29]
	v_mfma_f32_16x16x32_bf16 v[14:17], v[148:151], v[210:213], v[14:17]
	v_mfma_f32_16x16x32_bf16 v[10:13], v[156:159], v[210:213], v[10:13]
	s_setprio 0
	s_setprio 1
	v_mfma_f32_16x16x32_bf16 v[54:57], v[160:163], v[176:179], 0
	v_mfma_f32_16x16x32_bf16 v[50:53], v[168:171], v[176:179], 0
	v_mfma_f32_16x16x32_bf16 v[38:41], v[160:163], v[184:187], 0
	v_mfma_f32_16x16x32_bf16 v[34:37], v[168:171], v[184:187], 0
	v_mfma_f32_16x16x32_bf16 v[22:25], v[160:163], v[192:195], 0
	v_mfma_f32_16x16x32_bf16 v[18:21], v[168:171], v[192:195], 0
	v_mfma_f32_16x16x32_bf16 v[6:9], v[160:163], v[206:209], 0
	v_mfma_f32_16x16x32_bf16 v[2:5], v[168:171], v[206:209], 0
	v_mfma_f32_16x16x32_bf16 v[54:57], v[164:167], v[180:183], v[54:57]
	v_mfma_f32_16x16x32_bf16 v[50:53], v[172:175], v[180:183], v[50:53]
	v_mfma_f32_16x16x32_bf16 v[38:41], v[164:167], v[188:191], v[38:41]
	v_mfma_f32_16x16x32_bf16 v[34:37], v[172:175], v[188:191], v[34:37]
	v_mfma_f32_16x16x32_bf16 v[22:25], v[164:167], v[202:205], v[22:25]
	v_mfma_f32_16x16x32_bf16 v[18:21], v[172:175], v[202:205], v[18:21]
	v_mfma_f32_16x16x32_bf16 v[6:9], v[164:167], v[210:213], v[6:9]
	v_mfma_f32_16x16x32_bf16 v[2:5], v[172:175], v[210:213], v[2:5]
	s_setprio 0
	s_barrier
	s_add_i32 s35, 0, 0x18000
	s_add_i32 s56, 0, 0x1c000
	v_add_u32_e32 v156, s35, v141
	v_add_u32_e32 v172, s56, v141
	ds_read_b128 v[144:147], v156
	ds_read_b128 v[148:151], v156 offset:1024
	ds_read_b128 v[152:155], v156 offset:2048
	ds_read_b128 v[156:159], v156 offset:3072
	ds_read_b128 v[160:163], v172
	ds_read_b128 v[164:167], v172 offset:1024
	ds_read_b128 v[168:171], v172 offset:2048
	ds_read_b128 v[172:175], v172 offset:3072
	s_add_u32 s4, s4, s8
	s_addc_u32 s5, s5, s9
	s_mov_b32 m0, s43
	v_lshl_add_u64 v[236:237], s[4:5], 0, v[132:133]
	ds_read_b128 v[176:179], v143 offset:32768
	ds_read_b128 v[180:183], v143 offset:33792
	ds_read_b128 v[184:187], v143 offset:34816
	ds_read_b128 v[188:191], v143 offset:35840
	ds_read_b128 v[192:195], v143 offset:36864
	ds_read_b128 v[202:205], v143 offset:37888
	ds_read_b128 v[206:209], v143 offset:38912
	ds_read_b128 v[210:213], v143 offset:39936
	global_load_lds_dwordx4 v[236:237], off
	v_lshl_add_u64 v[236:237], s[4:5], 0, v[134:135]
	s_mov_b32 m0, s44
	s_nop 0
	global_load_lds_dwordx4 v[236:237], off
	s_waitcnt vmcnt(8)
	s_waitcnt lgkmcnt(0)
	s_barrier
	s_setprio 1
	s_waitcnt lgkmcnt(0)
	v_mfma_f32_16x16x32_bf16 v[122:125], v[144:147], v[176:179], v[122:125]
	v_mfma_f32_16x16x32_bf16 v[126:129], v[152:155], v[176:179], v[126:129]
	v_mfma_f32_16x16x32_bf16 v[110:113], v[144:147], v[184:187], v[110:113]
	v_mfma_f32_16x16x32_bf16 v[106:109], v[152:155], v[184:187], v[106:109]
	v_mfma_f32_16x16x32_bf16 v[94:97], v[144:147], v[192:195], v[94:97]
	v_mfma_f32_16x16x32_bf16 v[90:93], v[152:155], v[192:195], v[90:93]
	v_mfma_f32_16x16x32_bf16 v[78:81], v[144:147], v[206:209], v[78:81]
	v_mfma_f32_16x16x32_bf16 v[74:77], v[152:155], v[206:209], v[74:77]
	v_mfma_f32_16x16x32_bf16 v[122:125], v[148:151], v[180:183], v[122:125]
	v_mfma_f32_16x16x32_bf16 v[126:129], v[156:159], v[180:183], v[126:129]
	v_mfma_f32_16x16x32_bf16 v[110:113], v[148:151], v[188:191], v[110:113]
	v_mfma_f32_16x16x32_bf16 v[106:109], v[156:159], v[188:191], v[106:109]
	v_mfma_f32_16x16x32_bf16 v[94:97], v[148:151], v[202:205], v[94:97]
	v_mfma_f32_16x16x32_bf16 v[90:93], v[156:159], v[202:205], v[90:93]
	v_mfma_f32_16x16x32_bf16 v[78:81], v[148:151], v[210:213], v[78:81]
	v_mfma_f32_16x16x32_bf16 v[74:77], v[156:159], v[210:213], v[74:77]
	s_setprio 0
	s_setprio 1
	v_mfma_f32_16x16x32_bf16 v[118:121], v[160:163], v[176:179], v[118:121]
	v_mfma_f32_16x16x32_bf16 v[114:117], v[168:171], v[176:179], v[114:117]
	v_mfma_f32_16x16x32_bf16 v[102:105], v[160:163], v[184:187], v[102:105]
	v_mfma_f32_16x16x32_bf16 v[98:101], v[168:171], v[184:187], v[98:101]
	v_mfma_f32_16x16x32_bf16 v[86:89], v[160:163], v[192:195], v[86:89]
	v_mfma_f32_16x16x32_bf16 v[82:85], v[168:171], v[192:195], v[82:85]
	v_mfma_f32_16x16x32_bf16 v[70:73], v[160:163], v[206:209], v[70:73]
	v_mfma_f32_16x16x32_bf16 v[66:69], v[168:171], v[206:209], v[66:69]
	v_mfma_f32_16x16x32_bf16 v[118:121], v[164:167], v[180:183], v[118:121]
	v_mfma_f32_16x16x32_bf16 v[114:117], v[172:175], v[180:183], v[114:117]
	v_mfma_f32_16x16x32_bf16 v[102:105], v[164:167], v[188:191], v[102:105]
	v_mfma_f32_16x16x32_bf16 v[98:101], v[172:175], v[188:191], v[98:101]
	v_mfma_f32_16x16x32_bf16 v[86:89], v[164:167], v[202:205], v[86:89]
	v_mfma_f32_16x16x32_bf16 v[82:85], v[172:175], v[202:205], v[82:85]
	v_mfma_f32_16x16x32_bf16 v[70:73], v[164:167], v[210:213], v[70:73]
	v_mfma_f32_16x16x32_bf16 v[66:69], v[172:175], v[210:213], v[66:69]
	s_setprio 0
	s_barrier
	s_add_i32 s4, s35, s51
	v_lshl_add_u64 v[196:197], v[196:197], 0, s[94:95]
	s_mov_b32 m0, s4
	ds_read_b128 v[176:179], v143 offset:49152
	ds_read_b128 v[180:183], v143 offset:50176
	ds_read_b128 v[184:187], v143 offset:51200
	ds_read_b128 v[188:191], v143 offset:52224
	ds_read_b128 v[192:195], v143 offset:53248
	ds_read_b128 v[202:205], v143 offset:54272
	ds_read_b128 v[206:209], v143 offset:55296
	ds_read_b128 v[210:213], v143 offset:56320
	global_load_lds_dwordx4 v[196:197], off
	v_lshl_add_u64 v[196:197], v[214:215], 0, s[94:95]
	s_add_i32 m0, s4, 0x2000
	s_add_i32 s4, s56, s51
	global_load_lds_dwordx4 v[196:197], off
	v_lshl_add_u64 v[196:197], v[216:217], 0, s[94:95]
	s_mov_b32 m0, s4
	s_nop 0
	global_load_lds_dwordx4 v[196:197], off
	v_lshl_add_u64 v[196:197], v[218:219], 0, s[94:95]
	s_add_i32 m0, s4, 0x2000
	s_nop 0
	global_load_lds_dwordx4 v[196:197], off
	v_lshl_add_u64 v[196:197], v[220:221], 0, s[94:95]
	s_mov_b32 m0, s46
	s_nop 0
	global_load_lds_dwordx4 v[196:197], off
	v_lshl_add_u64 v[196:197], v[234:235], 0, s[94:95]
	s_mov_b32 m0, s47
	s_nop 0
	global_load_lds_dwordx4 v[196:197], off
	s_waitcnt vmcnt(8)
	s_waitcnt lgkmcnt(0)
	s_barrier
	s_setprio 1
	s_waitcnt lgkmcnt(0)
	v_mfma_f32_16x16x32_bf16 v[62:65], v[144:147], v[176:179], v[62:65]
	v_mfma_f32_16x16x32_bf16 v[58:61], v[152:155], v[176:179], v[58:61]
	v_mfma_f32_16x16x32_bf16 v[46:49], v[144:147], v[184:187], v[46:49]
	v_mfma_f32_16x16x32_bf16 v[42:45], v[152:155], v[184:187], v[42:45]
	v_mfma_f32_16x16x32_bf16 v[30:33], v[144:147], v[192:195], v[30:33]
	v_mfma_f32_16x16x32_bf16 v[26:29], v[152:155], v[192:195], v[26:29]
	v_mfma_f32_16x16x32_bf16 v[14:17], v[144:147], v[206:209], v[14:17]
	v_mfma_f32_16x16x32_bf16 v[10:13], v[152:155], v[206:209], v[10:13]
	v_mfma_f32_16x16x32_bf16 v[62:65], v[148:151], v[180:183], v[62:65]
	v_mfma_f32_16x16x32_bf16 v[58:61], v[156:159], v[180:183], v[58:61]
	v_mfma_f32_16x16x32_bf16 v[46:49], v[148:151], v[188:191], v[46:49]
	v_mfma_f32_16x16x32_bf16 v[42:45], v[156:159], v[188:191], v[42:45]
	v_mfma_f32_16x16x32_bf16 v[30:33], v[148:151], v[202:205], v[30:33]
	v_mfma_f32_16x16x32_bf16 v[26:29], v[156:159], v[202:205], v[26:29]
	v_mfma_f32_16x16x32_bf16 v[14:17], v[148:151], v[210:213], v[14:17]
	v_mfma_f32_16x16x32_bf16 v[10:13], v[156:159], v[210:213], v[10:13]
	s_setprio 0
	s_setprio 1
	v_mfma_f32_16x16x32_bf16 v[54:57], v[160:163], v[176:179], v[54:57]
	v_mfma_f32_16x16x32_bf16 v[50:53], v[168:171], v[176:179], v[50:53]
	v_mfma_f32_16x16x32_bf16 v[38:41], v[160:163], v[184:187], v[38:41]
	v_mfma_f32_16x16x32_bf16 v[34:37], v[168:171], v[184:187], v[34:37]
	v_mfma_f32_16x16x32_bf16 v[22:25], v[160:163], v[192:195], v[22:25]
	v_mfma_f32_16x16x32_bf16 v[18:21], v[168:171], v[192:195], v[18:21]
	v_mfma_f32_16x16x32_bf16 v[6:9], v[160:163], v[206:209], v[6:9]
	v_mfma_f32_16x16x32_bf16 v[2:5], v[168:171], v[206:209], v[2:5]
	v_mfma_f32_16x16x32_bf16 v[54:57], v[164:167], v[180:183], v[54:57]
	v_mfma_f32_16x16x32_bf16 v[50:53], v[172:175], v[180:183], v[50:53]
	v_mfma_f32_16x16x32_bf16 v[38:41], v[164:167], v[188:191], v[38:41]
	v_mfma_f32_16x16x32_bf16 v[34:37], v[172:175], v[188:191], v[34:37]
	v_mfma_f32_16x16x32_bf16 v[22:25], v[164:167], v[202:205], v[22:25]
	v_mfma_f32_16x16x32_bf16 v[18:21], v[172:175], v[202:205], v[18:21]
	v_mfma_f32_16x16x32_bf16 v[6:9], v[164:167], v[210:213], v[6:9]
	v_mfma_f32_16x16x32_bf16 v[2:5], v[172:175], v[210:213], v[2:5]
	s_setprio 0
	s_barrier
	s_add_u32 s30, s30, 0x100
	s_addc_u32 s31, s31, 0
	s_add_u32 s19, s19, 0x100
	s_addc_u32 s21, s21, 0
	s_cmp_ge_i32 s34, s45
	s_mov_b32 s4, s34
	s_cbranch_scc1 .LBB0_116

.LBB0_542:
	s_andn2_b64 vcc, exec, s[14:15]
	s_cbranch_vccnz .LBB0_546
	s_add_u32 s30, s30, 0x80
	s_addc_u32 s31, s31, 0
	s_add_u32 s19, s34, 0x100
	s_addc_u32 s21, s35, 0
	s_mov_b32 s4, 0
	s_add_i32 s34, s4, 2
	s_add_u32 s35, s30, 0x80
	s_addc_u32 s5, s31, 0
	s_add_i32 s51, 0, 0x10000
	s_cmp_eq_u32 s47, s4
	s_cselect_b32 s5, s27, s5
	s_cselect_b32 s4, s26, s35
	s_cselect_b32 s57, s29, s21
	s_cselect_b32 s56, s28, s19
	s_add_i32 s35, 0, 0x14000
	v_add_u32_e32 v156, s51, v141
	v_add_u32_e32 v172, s35, v141
	ds_read_b128 v[144:147], v156
	ds_read_b128 v[148:151], v156 offset:1024
	ds_read_b128 v[152:155], v156 offset:2048
	ds_read_b128 v[156:159], v156 offset:3072
	ds_read_b128 v[160:163], v172
	ds_read_b128 v[164:167], v172 offset:1024
	ds_read_b128 v[168:171], v172 offset:2048
	ds_read_b128 v[172:175], v172 offset:3072
	v_lshl_add_u64 v[196:197], s[30:31], 0, v[136:137]
	s_add_i32 m0, s40, 0xc000
	ds_read_b128 v[176:179], v143
	ds_read_b128 v[180:183], v143 offset:1024
	ds_read_b128 v[184:187], v143 offset:2048
	ds_read_b128 v[188:191], v143 offset:3072
	ds_read_b128 v[192:195], v143 offset:4096
	ds_read_b128 v[202:205], v143 offset:5120
	ds_read_b128 v[206:209], v143 offset:6144
	ds_read_b128 v[210:213], v143 offset:7168
	global_load_lds_dwordx4 v[196:197], off
	v_lshl_add_u64 v[196:197], s[30:31], 0, v[138:139]
	s_add_i32 m0, s40, 0xe000
	s_nop 0
	global_load_lds_dwordx4 v[196:197], off
	s_waitcnt vmcnt(24)
	s_waitcnt lgkmcnt(0)
	s_barrier
	s_setprio 1
	s_waitcnt lgkmcnt(0)
	v_mfma_f32_16x16x32_bf16 v[122:125], v[144:147], v[176:179], 0
	v_mfma_f32_16x16x32_bf16 v[126:129], v[152:155], v[176:179], 0
	v_mfma_f32_16x16x32_bf16 v[110:113], v[144:147], v[184:187], 0
	v_mfma_f32_16x16x32_bf16 v[106:109], v[152:155], v[184:187], 0
	v_mfma_f32_16x16x32_bf16 v[94:97], v[144:147], v[192:195], 0
	v_mfma_f32_16x16x32_bf16 v[90:93], v[152:155], v[192:195], 0
	v_mfma_f32_16x16x32_bf16 v[78:81], v[144:147], v[206:209], 0
	v_mfma_f32_16x16x32_bf16 v[74:77], v[152:155], v[206:209], 0
	v_mfma_f32_16x16x32_bf16 v[122:125], v[148:151], v[180:183], v[122:125]
	v_mfma_f32_16x16x32_bf16 v[126:129], v[156:159], v[180:183], v[126:129]
	v_mfma_f32_16x16x32_bf16 v[110:113], v[148:151], v[188:191], v[110:113]
	v_mfma_f32_16x16x32_bf16 v[106:109], v[156:159], v[188:191], v[106:109]
	v_mfma_f32_16x16x32_bf16 v[94:97], v[148:151], v[202:205], v[94:97]
	v_mfma_f32_16x16x32_bf16 v[90:93], v[156:159], v[202:205], v[90:93]
	v_mfma_f32_16x16x32_bf16 v[78:81], v[148:151], v[210:213], v[78:81]
	v_mfma_f32_16x16x32_bf16 v[74:77], v[156:159], v[210:213], v[74:77]
	s_setprio 0
	s_setprio 1
	v_mfma_f32_16x16x32_bf16 v[118:121], v[160:163], v[176:179], 0
	v_mfma_f32_16x16x32_bf16 v[114:117], v[168:171], v[176:179], 0
	v_mfma_f32_16x16x32_bf16 v[102:105], v[160:163], v[184:187], 0
	v_mfma_f32_16x16x32_bf16 v[98:101], v[168:171], v[184:187], 0
	v_mfma_f32_16x16x32_bf16 v[86:89], v[160:163], v[192:195], 0
	v_mfma_f32_16x16x32_bf16 v[82:85], v[168:171], v[192:195], 0
	v_mfma_f32_16x16x32_bf16 v[70:73], v[160:163], v[206:209], 0
	v_mfma_f32_16x16x32_bf16 v[66:69], v[168:171], v[206:209], 0
	v_mfma_f32_16x16x32_bf16 v[118:121], v[164:167], v[180:183], v[118:121]
	v_mfma_f32_16x16x32_bf16 v[114:117], v[172:175], v[180:183], v[114:117]
	v_mfma_f32_16x16x32_bf16 v[102:105], v[164:167], v[188:191], v[102:105]
	v_mfma_f32_16x16x32_bf16 v[98:101], v[172:175], v[188:191], v[98:101]
	v_mfma_f32_16x16x32_bf16 v[86:89], v[164:167], v[202:205], v[86:89]
	v_mfma_f32_16x16x32_bf16 v[82:85], v[172:175], v[202:205], v[82:85]
	v_mfma_f32_16x16x32_bf16 v[70:73], v[164:167], v[210:213], v[70:73]
	v_mfma_f32_16x16x32_bf16 v[66:69], v[172:175], v[210:213], v[66:69]
	s_setprio 0
	s_barrier
	s_add_i32 s51, s51, s39
	v_lshl_add_u64 v[196:197], s[56:57], 0, v[0:1]
	s_mov_b32 m0, s51
	ds_read_b128 v[176:179], v143 offset:16384
	ds_read_b128 v[180:183], v143 offset:17408
	ds_read_b128 v[184:187], v143 offset:18432
	ds_read_b128 v[188:191], v143 offset:19456
	ds_read_b128 v[192:195], v143 offset:20480
	ds_read_b128 v[202:205], v143 offset:21504
	ds_read_b128 v[206:209], v143 offset:22528
	ds_read_b128 v[210:213], v143 offset:23552
	global_load_lds_dwordx4 v[196:197], off
	s_add_i32 m0, s51, 0x2000
	v_lshl_add_u64 v[214:215], s[56:57], 0, v[130:131]
	s_add_u32 s56, s56, s8
	s_addc_u32 s57, s57, s9
	s_add_i32 s35, s35, s39
	global_load_lds_dwordx4 v[214:215], off
	v_lshl_add_u64 v[216:217], s[56:57], 0, v[0:1]
	s_mov_b32 m0, s35
	v_lshl_add_u64 v[218:219], s[56:57], 0, v[130:131]
	global_load_lds_dwordx4 v[216:217], off
	s_add_i32 m0, s35, 0x2000
	v_lshl_add_u64 v[220:221], s[4:5], 0, v[132:133]
	global_load_lds_dwordx4 v[218:219], off
	s_mov_b32 m0, s40
	v_lshl_add_u64 v[234:235], s[4:5], 0, v[134:135]
	global_load_lds_dwordx4 v[220:221], off
	s_mov_b32 m0, s41
	s_nop 0
	global_load_lds_dwordx4 v[234:235], off
	s_cmp_eq_u32 s48, 1
	s_cbranch_scc1 .Lfw_wo_8
	s_waitcnt vmcnt(24)
	s_branch .Lfw_wo_d
.Lfw_wo_8:
	s_waitcnt vmcnt(8)
.Lfw_wo_d:
	s_waitcnt lgkmcnt(0)
	s_barrier
	s_setprio 1
	s_waitcnt lgkmcnt(0)
	v_mfma_f32_16x16x32_bf16 v[62:65], v[144:147], v[176:179], 0
	v_mfma_f32_16x16x32_bf16 v[58:61], v[152:155], v[176:179], 0
	v_mfma_f32_16x16x32_bf16 v[46:49], v[144:147], v[184:187], 0
	v_mfma_f32_16x16x32_bf16 v[42:45], v[152:155], v[184:187], 0
	v_mfma_f32_16x16x32_bf16 v[30:33], v[144:147], v[192:195], 0
	v_mfma_f32_16x16x32_bf16 v[26:29], v[152:155], v[192:195], 0
	v_mfma_f32_16x16x32_bf16 v[14:17], v[144:147], v[206:209], 0
	v_mfma_f32_16x16x32_bf16 v[10:13], v[152:155], v[206:209], 0
	v_mfma_f32_16x16x32_bf16 v[62:65], v[148:151], v[180:183], v[62:65]
	v_mfma_f32_16x16x32_bf16 v[58:61], v[156:159], v[180:183], v[58:61]
	v_mfma_f32_16x16x32_bf16 v[46:49], v[148:151], v[188:191], v[46:49]
	v_mfma_f32_16x16x32_bf16 v[42:45], v[156:159], v[188:191], v[42:45]
	v_mfma_f32_16x16x32_bf16 v[30:33], v[148:151], v[202:205], v[30:33]
	v_mfma_f32_16x16x32_bf16 v[26:29], v[156:159], v[202:205], v[26:29]
	v_mfma_f32_16x16x32_bf16 v[14:17], v[148:151], v[210:213], v[14:17]
	v_mfma_f32_16x16x32_bf16 v[10:13], v[156:159], v[210:213], v[10:13]
	s_setprio 0
	s_setprio 1
	v_mfma_f32_16x16x32_bf16 v[54:57], v[160:163], v[176:179], 0
	v_mfma_f32_16x16x32_bf16 v[50:53], v[168:171], v[176:179], 0
	v_mfma_f32_16x16x32_bf16 v[38:41], v[160:163], v[184:187], 0
	v_mfma_f32_16x16x32_bf16 v[34:37], v[168:171], v[184:187], 0
	v_mfma_f32_16x16x32_bf16 v[22:25], v[160:163], v[192:195], 0
	v_mfma_f32_16x16x32_bf16 v[18:21], v[168:171], v[192:195], 0
	v_mfma_f32_16x16x32_bf16 v[6:9], v[160:163], v[206:209], 0
	v_mfma_f32_16x16x32_bf16 v[2:5], v[168:171], v[206:209], 0
	v_mfma_f32_16x16x32_bf16 v[54:57], v[164:167], v[180:183], v[54:57]
	v_mfma_f32_16x16x32_bf16 v[50:53], v[172:175], v[180:183], v[50:53]
	v_mfma_f32_16x16x32_bf16 v[38:41], v[164:167], v[188:191], v[38:41]
	v_mfma_f32_16x16x32_bf16 v[34:37], v[172:175], v[188:191], v[34:37]
	v_mfma_f32_16x16x32_bf16 v[22:25], v[164:167], v[202:205], v[22:25]
	v_mfma_f32_16x16x32_bf16 v[18:21], v[172:175], v[202:205], v[18:21]
	v_mfma_f32_16x16x32_bf16 v[6:9], v[164:167], v[210:213], v[6:9]
	v_mfma_f32_16x16x32_bf16 v[2:5], v[172:175], v[210:213], v[2:5]
	s_setprio 0
	s_barrier
	s_add_i32 s35, 0, 0x18000
	s_add_i32 s51, 0, 0x1c000
	v_add_u32_e32 v156, s35, v141
	v_add_u32_e32 v172, s51, v141
	ds_read_b128 v[144:147], v156
	ds_read_b128 v[148:151], v156 offset:1024
	ds_read_b128 v[152:155], v156 offset:2048
	ds_read_b128 v[156:159], v156 offset:3072
	ds_read_b128 v[160:163], v172
	ds_read_b128 v[164:167], v172 offset:1024
	ds_read_b128 v[168:171], v172 offset:2048
	ds_read_b128 v[172:175], v172 offset:3072
	s_add_u32 s4, s4, s8
	s_addc_u32 s5, s5, s9
	s_mov_b32 m0, s42
	v_lshl_add_u64 v[236:237], s[4:5], 0, v[132:133]
	ds_read_b128 v[176:179], v143 offset:32768
	ds_read_b128 v[180:183], v143 offset:33792
	ds_read_b128 v[184:187], v143 offset:34816
	ds_read_b128 v[188:191], v143 offset:35840
	ds_read_b128 v[192:195], v143 offset:36864
	ds_read_b128 v[202:205], v143 offset:37888
	ds_read_b128 v[206:209], v143 offset:38912
	ds_read_b128 v[210:213], v143 offset:39936
	global_load_lds_dwordx4 v[236:237], off
	v_lshl_add_u64 v[236:237], s[4:5], 0, v[134:135]
	s_mov_b32 m0, s43
	s_nop 0
	global_load_lds_dwordx4 v[236:237], off
	s_waitcnt vmcnt(8)
	s_waitcnt lgkmcnt(0)
	s_barrier
	s_setprio 1
	s_waitcnt lgkmcnt(0)
	v_mfma_f32_16x16x32_bf16 v[122:125], v[144:147], v[176:179], v[122:125]
	v_mfma_f32_16x16x32_bf16 v[126:129], v[152:155], v[176:179], v[126:129]
	v_mfma_f32_16x16x32_bf16 v[110:113], v[144:147], v[184:187], v[110:113]
	v_mfma_f32_16x16x32_bf16 v[106:109], v[152:155], v[184:187], v[106:109]
	v_mfma_f32_16x16x32_bf16 v[94:97], v[144:147], v[192:195], v[94:97]
	v_mfma_f32_16x16x32_bf16 v[90:93], v[152:155], v[192:195], v[90:93]
	v_mfma_f32_16x16x32_bf16 v[78:81], v[144:147], v[206:209], v[78:81]
	v_mfma_f32_16x16x32_bf16 v[74:77], v[152:155], v[206:209], v[74:77]
	v_mfma_f32_16x16x32_bf16 v[122:125], v[148:151], v[180:183], v[122:125]
	v_mfma_f32_16x16x32_bf16 v[126:129], v[156:159], v[180:183], v[126:129]
	v_mfma_f32_16x16x32_bf16 v[110:113], v[148:151], v[188:191], v[110:113]
	v_mfma_f32_16x16x32_bf16 v[106:109], v[156:159], v[188:191], v[106:109]
	v_mfma_f32_16x16x32_bf16 v[94:97], v[148:151], v[202:205], v[94:97]
	v_mfma_f32_16x16x32_bf16 v[90:93], v[156:159], v[202:205], v[90:93]
	v_mfma_f32_16x16x32_bf16 v[78:81], v[148:151], v[210:213], v[78:81]
	v_mfma_f32_16x16x32_bf16 v[74:77], v[156:159], v[210:213], v[74:77]
	s_setprio 0
	s_setprio 1
	v_mfma_f32_16x16x32_bf16 v[118:121], v[160:163], v[176:179], v[118:121]
	v_mfma_f32_16x16x32_bf16 v[114:117], v[168:171], v[176:179], v[114:117]
	v_mfma_f32_16x16x32_bf16 v[102:105], v[160:163], v[184:187], v[102:105]
	v_mfma_f32_16x16x32_bf16 v[98:101], v[168:171], v[184:187], v[98:101]
	v_mfma_f32_16x16x32_bf16 v[86:89], v[160:163], v[192:195], v[86:89]
	v_mfma_f32_16x16x32_bf16 v[82:85], v[168:171], v[192:195], v[82:85]
	v_mfma_f32_16x16x32_bf16 v[70:73], v[160:163], v[206:209], v[70:73]
	v_mfma_f32_16x16x32_bf16 v[66:69], v[168:171], v[206:209], v[66:69]
	v_mfma_f32_16x16x32_bf16 v[118:121], v[164:167], v[180:183], v[118:121]
	v_mfma_f32_16x16x32_bf16 v[114:117], v[172:175], v[180:183], v[114:117]
	v_mfma_f32_16x16x32_bf16 v[102:105], v[164:167], v[188:191], v[102:105]
	v_mfma_f32_16x16x32_bf16 v[98:101], v[172:175], v[188:191], v[98:101]
	v_mfma_f32_16x16x32_bf16 v[86:89], v[164:167], v[202:205], v[86:89]
	v_mfma_f32_16x16x32_bf16 v[82:85], v[172:175], v[202:205], v[82:85]
	v_mfma_f32_16x16x32_bf16 v[70:73], v[164:167], v[210:213], v[70:73]
	v_mfma_f32_16x16x32_bf16 v[66:69], v[172:175], v[210:213], v[66:69]
	s_setprio 0
	s_barrier
	s_add_i32 s4, s35, s39
	v_lshl_add_u64 v[196:197], v[196:197], 0, s[94:95]
	s_mov_b32 m0, s4
	ds_read_b128 v[176:179], v143 offset:49152
	ds_read_b128 v[180:183], v143 offset:50176
	ds_read_b128 v[184:187], v143 offset:51200
	ds_read_b128 v[188:191], v143 offset:52224
	ds_read_b128 v[192:195], v143 offset:53248
	ds_read_b128 v[202:205], v143 offset:54272
	ds_read_b128 v[206:209], v143 offset:55296
	ds_read_b128 v[210:213], v143 offset:56320
	global_load_lds_dwordx4 v[196:197], off
	v_lshl_add_u64 v[196:197], v[214:215], 0, s[94:95]
	s_add_i32 m0, s4, 0x2000
	s_add_i32 s4, s51, s39
	global_load_lds_dwordx4 v[196:197], off
	v_lshl_add_u64 v[196:197], v[216:217], 0, s[94:95]
	s_mov_b32 m0, s4
	s_nop 0
	global_load_lds_dwordx4 v[196:197], off
	v_lshl_add_u64 v[196:197], v[218:219], 0, s[94:95]
	s_add_i32 m0, s4, 0x2000
	s_nop 0
	global_load_lds_dwordx4 v[196:197], off
	v_lshl_add_u64 v[196:197], v[220:221], 0, s[94:95]
	s_mov_b32 m0, s45
	s_nop 0
	global_load_lds_dwordx4 v[196:197], off
	v_lshl_add_u64 v[196:197], v[234:235], 0, s[94:95]
	s_mov_b32 m0, s46
	s_nop 0
	global_load_lds_dwordx4 v[196:197], off
	s_waitcnt vmcnt(8)
	s_waitcnt lgkmcnt(0)
	s_barrier
	s_setprio 1
	s_waitcnt lgkmcnt(0)
	v_mfma_f32_16x16x32_bf16 v[62:65], v[144:147], v[176:179], v[62:65]
	v_mfma_f32_16x16x32_bf16 v[58:61], v[152:155], v[176:179], v[58:61]
	v_mfma_f32_16x16x32_bf16 v[46:49], v[144:147], v[184:187], v[46:49]
	v_mfma_f32_16x16x32_bf16 v[42:45], v[152:155], v[184:187], v[42:45]
	v_mfma_f32_16x16x32_bf16 v[30:33], v[144:147], v[192:195], v[30:33]
	v_mfma_f32_16x16x32_bf16 v[26:29], v[152:155], v[192:195], v[26:29]
	v_mfma_f32_16x16x32_bf16 v[14:17], v[144:147], v[206:209], v[14:17]
	v_mfma_f32_16x16x32_bf16 v[10:13], v[152:155], v[206:209], v[10:13]
	v_mfma_f32_16x16x32_bf16 v[62:65], v[148:151], v[180:183], v[62:65]
	v_mfma_f32_16x16x32_bf16 v[58:61], v[156:159], v[180:183], v[58:61]
	v_mfma_f32_16x16x32_bf16 v[46:49], v[148:151], v[188:191], v[46:49]
	v_mfma_f32_16x16x32_bf16 v[42:45], v[156:159], v[188:191], v[42:45]
	v_mfma_f32_16x16x32_bf16 v[30:33], v[148:151], v[202:205], v[30:33]
	v_mfma_f32_16x16x32_bf16 v[26:29], v[156:159], v[202:205], v[26:29]
	v_mfma_f32_16x16x32_bf16 v[14:17], v[148:151], v[210:213], v[14:17]
	v_mfma_f32_16x16x32_bf16 v[10:13], v[156:159], v[210:213], v[10:13]
	s_setprio 0
	s_setprio 1
	v_mfma_f32_16x16x32_bf16 v[54:57], v[160:163], v[176:179], v[54:57]
	v_mfma_f32_16x16x32_bf16 v[50:53], v[168:171], v[176:179], v[50:53]
	v_mfma_f32_16x16x32_bf16 v[38:41], v[160:163], v[184:187], v[38:41]
	v_mfma_f32_16x16x32_bf16 v[34:37], v[168:171], v[184:187], v[34:37]
	v_mfma_f32_16x16x32_bf16 v[22:25], v[160:163], v[192:195], v[22:25]
	v_mfma_f32_16x16x32_bf16 v[18:21], v[168:171], v[192:195], v[18:21]
	v_mfma_f32_16x16x32_bf16 v[6:9], v[160:163], v[206:209], v[6:9]
	v_mfma_f32_16x16x32_bf16 v[2:5], v[168:171], v[206:209], v[2:5]
	v_mfma_f32_16x16x32_bf16 v[54:57], v[164:167], v[180:183], v[54:57]
	v_mfma_f32_16x16x32_bf16 v[50:53], v[172:175], v[180:183], v[50:53]
	v_mfma_f32_16x16x32_bf16 v[38:41], v[164:167], v[188:191], v[38:41]
	v_mfma_f32_16x16x32_bf16 v[34:37], v[172:175], v[188:191], v[34:37]
	v_mfma_f32_16x16x32_bf16 v[22:25], v[164:167], v[202:205], v[22:25]
	v_mfma_f32_16x16x32_bf16 v[18:21], v[172:175], v[202:205], v[18:21]
	v_mfma_f32_16x16x32_bf16 v[6:9], v[164:167], v[210:213], v[6:9]
	v_mfma_f32_16x16x32_bf16 v[2:5], v[172:175], v[210:213], v[2:5]
	s_setprio 0
	s_barrier
	s_add_u32 s30, s30, 0x100
	s_addc_u32 s31, s31, 0
	s_add_u32 s19, s19, 0x100
	s_addc_u32 s21, s21, 0
	s_cmp_ge_i32 s34, s44
	s_mov_b32 s4, s34
	s_cbranch_scc1 .Lpeel_exit_2

.LBB0_838:
	s_andn2_b64 vcc, exec, s[14:15]
	s_cbranch_vccnz .LBB0_841
	s_add_u32 s24, s24, 0x80
	s_addc_u32 s25, s25, 0
	s_add_u32 s26, s26, 0x100
	s_addc_u32 s27, s27, 0
	s_mov_b32 s4, 0
	s_add_i32 s46, s4, 2
	s_add_u32 s47, s24, 0x80
	s_addc_u32 s5, s25, 0
	s_add_i32 s50, 0, 0x10000
	s_cmp_eq_u32 s41, s4
	s_cselect_b32 s5, s21, s5
	s_cselect_b32 s4, s20, s47
	v_add_u32_e32 v145, s50, v142
	s_cselect_b32 s49, s23, s27
	s_cselect_b32 s48, s22, s26
	s_add_i32 s47, 0, 0x14000
	ds_read_b128 v[146:149], v145
	ds_read_b128 v[150:153], v145 offset:1024
	ds_read_b128 v[154:157], v145 offset:2048
	ds_read_b128 v[158:161], v145 offset:3072
	v_add_u32_e32 v145, s47, v142
	ds_read_b128 v[162:165], v145
	ds_read_b128 v[166:169], v145 offset:1024
	ds_read_b128 v[170:173], v145 offset:2048
	ds_read_b128 v[174:177], v145 offset:3072
	v_lshl_add_u64 v[214:215], s[24:25], 0, v[136:137]
	s_add_i32 m0, s34, 0xc000
	ds_read_b128 v[178:181], v144
	ds_read_b128 v[182:185], v144 offset:1024
	ds_read_b128 v[186:189], v144 offset:2048
	ds_read_b128 v[190:193], v144 offset:3072
	ds_read_b128 v[194:197], v144 offset:4096
	ds_read_b128 v[202:205], v144 offset:5120
	ds_read_b128 v[206:209], v144 offset:6144
	ds_read_b128 v[210:213], v144 offset:7168
	global_load_lds_dwordx4 v[214:215], off
	v_lshl_add_u64 v[214:215], s[24:25], 0, v[138:139]
	s_add_i32 m0, s34, 0xe000
	s_nop 0
	global_load_lds_dwordx4 v[214:215], off
	s_waitcnt vmcnt(16)
	s_waitcnt lgkmcnt(0)
	s_barrier
	s_setprio 1
	s_waitcnt lgkmcnt(0)
	v_mfma_f32_16x16x32_bf16 v[126:129], v[146:149], v[178:181], 0
	v_mfma_f32_16x16x32_bf16 v[122:125], v[154:157], v[178:181], 0
	v_mfma_f32_16x16x32_bf16 v[110:113], v[146:149], v[186:189], 0
	v_mfma_f32_16x16x32_bf16 v[106:109], v[154:157], v[186:189], 0
	v_mfma_f32_16x16x32_bf16 v[94:97], v[146:149], v[194:197], 0
	v_mfma_f32_16x16x32_bf16 v[90:93], v[154:157], v[194:197], 0
	v_mfma_f32_16x16x32_bf16 v[78:81], v[146:149], v[206:209], 0
	v_mfma_f32_16x16x32_bf16 v[74:77], v[154:157], v[206:209], 0
	v_mfma_f32_16x16x32_bf16 v[126:129], v[150:153], v[182:185], v[126:129]
	v_mfma_f32_16x16x32_bf16 v[122:125], v[158:161], v[182:185], v[122:125]
	v_mfma_f32_16x16x32_bf16 v[110:113], v[150:153], v[190:193], v[110:113]
	v_mfma_f32_16x16x32_bf16 v[106:109], v[158:161], v[190:193], v[106:109]
	v_mfma_f32_16x16x32_bf16 v[94:97], v[150:153], v[202:205], v[94:97]
	v_mfma_f32_16x16x32_bf16 v[90:93], v[158:161], v[202:205], v[90:93]
	v_mfma_f32_16x16x32_bf16 v[78:81], v[150:153], v[210:213], v[78:81]
	v_mfma_f32_16x16x32_bf16 v[74:77], v[158:161], v[210:213], v[74:77]
	s_setprio 0
	s_setprio 1
	v_mfma_f32_16x16x32_bf16 v[118:121], v[162:165], v[178:181], 0
	v_mfma_f32_16x16x32_bf16 v[114:117], v[170:173], v[178:181], 0
	v_mfma_f32_16x16x32_bf16 v[102:105], v[162:165], v[186:189], 0
	v_mfma_f32_16x16x32_bf16 v[98:101], v[170:173], v[186:189], 0
	v_mfma_f32_16x16x32_bf16 v[86:89], v[162:165], v[194:197], 0
	v_mfma_f32_16x16x32_bf16 v[82:85], v[170:173], v[194:197], 0
	v_mfma_f32_16x16x32_bf16 v[70:73], v[162:165], v[206:209], 0
	v_mfma_f32_16x16x32_bf16 v[66:69], v[170:173], v[206:209], 0
	v_mfma_f32_16x16x32_bf16 v[118:121], v[166:169], v[182:185], v[118:121]
	v_mfma_f32_16x16x32_bf16 v[114:117], v[174:177], v[182:185], v[114:117]
	v_mfma_f32_16x16x32_bf16 v[102:105], v[166:169], v[190:193], v[102:105]
	v_mfma_f32_16x16x32_bf16 v[98:101], v[174:177], v[190:193], v[98:101]
	v_mfma_f32_16x16x32_bf16 v[86:89], v[166:169], v[202:205], v[86:89]
	v_mfma_f32_16x16x32_bf16 v[82:85], v[174:177], v[202:205], v[82:85]
	v_mfma_f32_16x16x32_bf16 v[70:73], v[166:169], v[210:213], v[70:73]
	v_mfma_f32_16x16x32_bf16 v[66:69], v[174:177], v[210:213], v[66:69]
	s_setprio 0
	s_barrier
	s_add_i32 s50, s50, s31
	v_lshl_add_u64 v[214:215], s[48:49], 0, v[0:1]
	s_mov_b32 m0, s50
	ds_read_b128 v[178:181], v144 offset:16384
	ds_read_b128 v[182:185], v144 offset:17408
	ds_read_b128 v[186:189], v144 offset:18432
	ds_read_b128 v[190:193], v144 offset:19456
	ds_read_b128 v[194:197], v144 offset:20480
	ds_read_b128 v[202:205], v144 offset:21504
	ds_read_b128 v[206:209], v144 offset:22528
	ds_read_b128 v[210:213], v144 offset:23552
	global_load_lds_dwordx4 v[214:215], off
	s_add_i32 m0, s50, 0x2000
	v_lshl_add_u64 v[216:217], s[48:49], 0, v[130:131]
	s_add_u32 s48, s48, s8
	s_addc_u32 s49, s49, s9
	s_add_i32 s47, s47, s31
	global_load_lds_dwordx4 v[216:217], off
	v_lshl_add_u64 v[218:219], s[48:49], 0, v[0:1]
	s_mov_b32 m0, s47
	v_lshl_add_u64 v[220:221], s[48:49], 0, v[130:131]
	global_load_lds_dwordx4 v[218:219], off
	s_add_i32 m0, s47, 0x2000
	v_lshl_add_u64 v[234:235], s[4:5], 0, v[132:133]
	global_load_lds_dwordx4 v[220:221], off
	s_mov_b32 m0, s34
	v_lshl_add_u64 v[236:237], s[4:5], 0, v[134:135]
	global_load_lds_dwordx4 v[234:235], off
	s_mov_b32 m0, s35
	s_nop 0
	global_load_lds_dwordx4 v[236:237], off
	s_cmp_eq_u32 s42, 1
	s_cbranch_scc1 .Lfw_dn_8
	s_waitcnt vmcnt(16)
	s_branch .Lfw_dn_d
.Lfw_dn_8:
	s_waitcnt vmcnt(8)
.Lfw_dn_d:
	s_waitcnt lgkmcnt(0)
	s_barrier
	s_setprio 1
	s_waitcnt lgkmcnt(0)
	v_mfma_f32_16x16x32_bf16 v[62:65], v[146:149], v[178:181], 0
	v_mfma_f32_16x16x32_bf16 v[58:61], v[154:157], v[178:181], 0
	v_mfma_f32_16x16x32_bf16 v[46:49], v[146:149], v[186:189], 0
	v_mfma_f32_16x16x32_bf16 v[42:45], v[154:157], v[186:189], 0
	v_mfma_f32_16x16x32_bf16 v[30:33], v[146:149], v[194:197], 0
	v_mfma_f32_16x16x32_bf16 v[26:29], v[154:157], v[194:197], 0
	v_mfma_f32_16x16x32_bf16 v[14:17], v[146:149], v[206:209], 0
	v_mfma_f32_16x16x32_bf16 v[10:13], v[154:157], v[206:209], 0
	v_mfma_f32_16x16x32_bf16 v[62:65], v[150:153], v[182:185], v[62:65]
	v_mfma_f32_16x16x32_bf16 v[58:61], v[158:161], v[182:185], v[58:61]
	v_mfma_f32_16x16x32_bf16 v[46:49], v[150:153], v[190:193], v[46:49]
	v_mfma_f32_16x16x32_bf16 v[42:45], v[158:161], v[190:193], v[42:45]
	v_mfma_f32_16x16x32_bf16 v[30:33], v[150:153], v[202:205], v[30:33]
	v_mfma_f32_16x16x32_bf16 v[26:29], v[158:161], v[202:205], v[26:29]
	v_mfma_f32_16x16x32_bf16 v[14:17], v[150:153], v[210:213], v[14:17]
	v_mfma_f32_16x16x32_bf16 v[10:13], v[158:161], v[210:213], v[10:13]
	s_setprio 0
	s_setprio 1
	v_mfma_f32_16x16x32_bf16 v[54:57], v[162:165], v[178:181], 0
	v_mfma_f32_16x16x32_bf16 v[50:53], v[170:173], v[178:181], 0
	v_mfma_f32_16x16x32_bf16 v[38:41], v[162:165], v[186:189], 0
	v_mfma_f32_16x16x32_bf16 v[34:37], v[170:173], v[186:189], 0
	v_mfma_f32_16x16x32_bf16 v[22:25], v[162:165], v[194:197], 0
	v_mfma_f32_16x16x32_bf16 v[18:21], v[170:173], v[194:197], 0
	v_mfma_f32_16x16x32_bf16 v[6:9], v[162:165], v[206:209], 0
	v_mfma_f32_16x16x32_bf16 v[2:5], v[170:173], v[206:209], 0
	v_mfma_f32_16x16x32_bf16 v[54:57], v[166:169], v[182:185], v[54:57]
	v_mfma_f32_16x16x32_bf16 v[50:53], v[174:177], v[182:185], v[50:53]
	v_mfma_f32_16x16x32_bf16 v[38:41], v[166:169], v[190:193], v[38:41]
	v_mfma_f32_16x16x32_bf16 v[34:37], v[174:177], v[190:193], v[34:37]
	v_mfma_f32_16x16x32_bf16 v[22:25], v[166:169], v[202:205], v[22:25]
	v_mfma_f32_16x16x32_bf16 v[18:21], v[174:177], v[202:205], v[18:21]
	v_mfma_f32_16x16x32_bf16 v[6:9], v[166:169], v[210:213], v[6:9]
	v_mfma_f32_16x16x32_bf16 v[2:5], v[174:177], v[210:213], v[2:5]
	s_setprio 0
	s_barrier
	s_add_i32 s47, 0, 0x18000
	v_add_u32_e32 v145, s47, v142
	s_add_i32 s48, 0, 0x1c000
	ds_read_b128 v[146:149], v145
	ds_read_b128 v[150:153], v145 offset:1024
	ds_read_b128 v[154:157], v145 offset:2048
	ds_read_b128 v[158:161], v145 offset:3072
	v_add_u32_e32 v145, s48, v142
	ds_read_b128 v[162:165], v145
	ds_read_b128 v[166:169], v145 offset:1024
	ds_read_b128 v[170:173], v145 offset:2048
	ds_read_b128 v[174:177], v145 offset:3072
	s_add_u32 s4, s4, s8
	s_addc_u32 s5, s5, s9
	s_mov_b32 m0, s36
	v_lshl_add_u64 v[238:239], s[4:5], 0, v[132:133]
	ds_read_b128 v[178:181], v144 offset:32768
	ds_read_b128 v[182:185], v144 offset:33792
	ds_read_b128 v[186:189], v144 offset:34816
	ds_read_b128 v[190:193], v144 offset:35840
	ds_read_b128 v[194:197], v144 offset:36864
	ds_read_b128 v[202:205], v144 offset:37888
	ds_read_b128 v[206:209], v144 offset:38912
	ds_read_b128 v[210:213], v144 offset:39936
	global_load_lds_dwordx4 v[238:239], off
	v_lshl_add_u64 v[238:239], s[4:5], 0, v[134:135]
	s_mov_b32 m0, s37
	s_nop 0
	global_load_lds_dwordx4 v[238:239], off
	s_waitcnt vmcnt(8)
	s_waitcnt lgkmcnt(0)
	s_barrier
	s_setprio 1
	s_waitcnt lgkmcnt(0)
	v_mfma_f32_16x16x32_bf16 v[126:129], v[146:149], v[178:181], v[126:129]
	v_mfma_f32_16x16x32_bf16 v[122:125], v[154:157], v[178:181], v[122:125]
	v_mfma_f32_16x16x32_bf16 v[110:113], v[146:149], v[186:189], v[110:113]
	v_mfma_f32_16x16x32_bf16 v[106:109], v[154:157], v[186:189], v[106:109]
	v_mfma_f32_16x16x32_bf16 v[94:97], v[146:149], v[194:197], v[94:97]
	v_mfma_f32_16x16x32_bf16 v[90:93], v[154:157], v[194:197], v[90:93]
	v_mfma_f32_16x16x32_bf16 v[78:81], v[146:149], v[206:209], v[78:81]
	v_mfma_f32_16x16x32_bf16 v[74:77], v[154:157], v[206:209], v[74:77]
	v_mfma_f32_16x16x32_bf16 v[126:129], v[150:153], v[182:185], v[126:129]
	v_mfma_f32_16x16x32_bf16 v[122:125], v[158:161], v[182:185], v[122:125]
	v_mfma_f32_16x16x32_bf16 v[110:113], v[150:153], v[190:193], v[110:113]
	v_mfma_f32_16x16x32_bf16 v[106:109], v[158:161], v[190:193], v[106:109]
	v_mfma_f32_16x16x32_bf16 v[94:97], v[150:153], v[202:205], v[94:97]
	v_mfma_f32_16x16x32_bf16 v[90:93], v[158:161], v[202:205], v[90:93]
	v_mfma_f32_16x16x32_bf16 v[78:81], v[150:153], v[210:213], v[78:81]
	v_mfma_f32_16x16x32_bf16 v[74:77], v[158:161], v[210:213], v[74:77]
	s_setprio 0
	s_setprio 1
	v_mfma_f32_16x16x32_bf16 v[118:121], v[162:165], v[178:181], v[118:121]
	v_mfma_f32_16x16x32_bf16 v[114:117], v[170:173], v[178:181], v[114:117]
	v_mfma_f32_16x16x32_bf16 v[102:105], v[162:165], v[186:189], v[102:105]
	v_mfma_f32_16x16x32_bf16 v[98:101], v[170:173], v[186:189], v[98:101]
	v_mfma_f32_16x16x32_bf16 v[86:89], v[162:165], v[194:197], v[86:89]
	v_mfma_f32_16x16x32_bf16 v[82:85], v[170:173], v[194:197], v[82:85]
	v_mfma_f32_16x16x32_bf16 v[70:73], v[162:165], v[206:209], v[70:73]
	v_mfma_f32_16x16x32_bf16 v[66:69], v[170:173], v[206:209], v[66:69]
	v_mfma_f32_16x16x32_bf16 v[118:121], v[166:169], v[182:185], v[118:121]
	v_mfma_f32_16x16x32_bf16 v[114:117], v[174:177], v[182:185], v[114:117]
	v_mfma_f32_16x16x32_bf16 v[102:105], v[166:169], v[190:193], v[102:105]
	v_mfma_f32_16x16x32_bf16 v[98:101], v[174:177], v[190:193], v[98:101]
	v_mfma_f32_16x16x32_bf16 v[86:89], v[166:169], v[202:205], v[86:89]
	v_mfma_f32_16x16x32_bf16 v[82:85], v[174:177], v[202:205], v[82:85]
	v_mfma_f32_16x16x32_bf16 v[70:73], v[166:169], v[210:213], v[70:73]
	v_mfma_f32_16x16x32_bf16 v[66:69], v[174:177], v[210:213], v[66:69]
	s_setprio 0
	s_barrier
	s_add_i32 s4, s47, s31
	v_lshl_add_u64 v[214:215], v[214:215], 0, s[94:95]
	s_mov_b32 m0, s4
	ds_read_b128 v[178:181], v144 offset:49152
	ds_read_b128 v[182:185], v144 offset:50176
	ds_read_b128 v[186:189], v144 offset:51200
	ds_read_b128 v[190:193], v144 offset:52224
	ds_read_b128 v[194:197], v144 offset:53248
	ds_read_b128 v[202:205], v144 offset:54272
	ds_read_b128 v[206:209], v144 offset:55296
	ds_read_b128 v[210:213], v144 offset:56320
	global_load_lds_dwordx4 v[214:215], off
	v_lshl_add_u64 v[214:215], v[216:217], 0, s[94:95]
	s_add_i32 m0, s4, 0x2000
	s_add_i32 s4, s48, s31
	global_load_lds_dwordx4 v[214:215], off
	v_lshl_add_u64 v[214:215], v[218:219], 0, s[94:95]
	s_mov_b32 m0, s4
	s_nop 0
	global_load_lds_dwordx4 v[214:215], off
	v_lshl_add_u64 v[214:215], v[220:221], 0, s[94:95]
	s_add_i32 m0, s4, 0x2000
	s_nop 0
	global_load_lds_dwordx4 v[214:215], off
	v_lshl_add_u64 v[214:215], v[234:235], 0, s[94:95]
	s_mov_b32 m0, s39
	s_nop 0
	global_load_lds_dwordx4 v[214:215], off
	v_lshl_add_u64 v[214:215], v[236:237], 0, s[94:95]
	s_mov_b32 m0, s40
	s_nop 0
	global_load_lds_dwordx4 v[214:215], off
	s_waitcnt vmcnt(8)
	s_waitcnt lgkmcnt(0)
	s_barrier
	s_setprio 1
	s_waitcnt lgkmcnt(0)
	v_mfma_f32_16x16x32_bf16 v[62:65], v[146:149], v[178:181], v[62:65]
	v_mfma_f32_16x16x32_bf16 v[58:61], v[154:157], v[178:181], v[58:61]
	v_mfma_f32_16x16x32_bf16 v[46:49], v[146:149], v[186:189], v[46:49]
	v_mfma_f32_16x16x32_bf16 v[42:45], v[154:157], v[186:189], v[42:45]
	v_mfma_f32_16x16x32_bf16 v[30:33], v[146:149], v[194:197], v[30:33]
	v_mfma_f32_16x16x32_bf16 v[26:29], v[154:157], v[194:197], v[26:29]
	v_mfma_f32_16x16x32_bf16 v[14:17], v[146:149], v[206:209], v[14:17]
	v_mfma_f32_16x16x32_bf16 v[10:13], v[154:157], v[206:209], v[10:13]
	v_mfma_f32_16x16x32_bf16 v[62:65], v[150:153], v[182:185], v[62:65]
	v_mfma_f32_16x16x32_bf16 v[58:61], v[158:161], v[182:185], v[58:61]
	v_mfma_f32_16x16x32_bf16 v[46:49], v[150:153], v[190:193], v[46:49]
	v_mfma_f32_16x16x32_bf16 v[42:45], v[158:161], v[190:193], v[42:45]
	v_mfma_f32_16x16x32_bf16 v[30:33], v[150:153], v[202:205], v[30:33]
	v_mfma_f32_16x16x32_bf16 v[26:29], v[158:161], v[202:205], v[26:29]
	v_mfma_f32_16x16x32_bf16 v[14:17], v[150:153], v[210:213], v[14:17]
	v_mfma_f32_16x16x32_bf16 v[10:13], v[158:161], v[210:213], v[10:13]
	s_setprio 0
	s_setprio 1
	v_mfma_f32_16x16x32_bf16 v[54:57], v[162:165], v[178:181], v[54:57]
	v_mfma_f32_16x16x32_bf16 v[50:53], v[170:173], v[178:181], v[50:53]
	v_mfma_f32_16x16x32_bf16 v[38:41], v[162:165], v[186:189], v[38:41]
	v_mfma_f32_16x16x32_bf16 v[34:37], v[170:173], v[186:189], v[34:37]
	v_mfma_f32_16x16x32_bf16 v[22:25], v[162:165], v[194:197], v[22:25]
	v_mfma_f32_16x16x32_bf16 v[18:21], v[170:173], v[194:197], v[18:21]
	v_mfma_f32_16x16x32_bf16 v[6:9], v[162:165], v[206:209], v[6:9]
	v_mfma_f32_16x16x32_bf16 v[2:5], v[170:173], v[206:209], v[2:5]
	v_mfma_f32_16x16x32_bf16 v[54:57], v[166:169], v[182:185], v[54:57]
	v_mfma_f32_16x16x32_bf16 v[50:53], v[174:177], v[182:185], v[50:53]
	v_mfma_f32_16x16x32_bf16 v[38:41], v[166:169], v[190:193], v[38:41]
	v_mfma_f32_16x16x32_bf16 v[34:37], v[174:177], v[190:193], v[34:37]
	v_mfma_f32_16x16x32_bf16 v[22:25], v[166:169], v[202:205], v[22:25]
	v_mfma_f32_16x16x32_bf16 v[18:21], v[174:177], v[202:205], v[18:21]
	v_mfma_f32_16x16x32_bf16 v[6:9], v[166:169], v[210:213], v[6:9]
	v_mfma_f32_16x16x32_bf16 v[2:5], v[174:177], v[210:213], v[2:5]
	s_setprio 0
	s_barrier
	s_add_u32 s24, s24, 0x100
	s_addc_u32 s25, s25, 0
	s_add_u32 s26, s26, 0x100
	s_addc_u32 s27, s27, 0
	s_cmp_ge_i32 s46, s38
	s_mov_b32 s4, s46
	s_cbranch_scc1 .LBB0_841
